# attention: split packed v_pk_add_f32 (score minus running max) into scalar v_sub_f32 pairs
# baseline (speedup 1.0000x reference)
; __device__ __forceinline__ void cmask(f32x16& p0, f32x16& p1, int jb, int qrel, int hi) {
;     const float NEG = -INFINITY; int kb = 64 * jb + 4 * hi;
; #pragma unroll
;     for (int r = 0; r < 16; ++r) { int kv = kb + (r & 3) + 8 * (r >> 2); if (kv > qrel) p0[r] = NEG; if (kv + 32 > qrel) p1[r] = NEG; }
; }
; __device__ __forceinline__ void glds16(const void* gsrc, unsigned lds_dst) { unsigned keep;
;     asm volatile("s_mov_b32 %0, m0\n\ts_mov_b32 m0, %2\n\ts_nop 0\n\tglobal_load_lds_dwordx4 %1, off\n\ts_mov_b32 m0, %0" : "=&s"(keep) : "v"(gsrc), "s"(lds_dst) : "memory"); }
; __device__ __forceinline__ float max3f(float a, float b, float c) { float r; asm("v_max3_f32 %0, %1, %2, %3" : "=v"(r) : "v"(a), "v"(b), "v"(c)); return r; }
; __device__ __forceinline__ float max2f(float a, float b) { float r; asm("v_max_f32_e32 %0, %1, %2" : "=v"(r) : "v"(a), "v"(b)); return r; }
; __device__ __forceinline__ float fadd_s(float a, float b) { float r; asm("v_add_f32_e32 %0, %1, %2" : "=v"(r) : "v"(a), "v"(b)); return r; }
; __device__ __forceinline__ float fsub_s(float a, float b) { float r; asm("v_sub_f32_e32 %0, %1, %2" : "=v"(r) : "v"(a), "v"(b)); return r; }
; __device__ __forceinline__ unsigned cvtpk_s(float lo, float hi) { return pg8::cvt_pk_f16(lo, hi); }
; __device__ __forceinline__ void qkt(f32x16& p0, f32x16& p1, const char* Kslot, const s16x8* qr, const f32x16& negm, int r32, int hi) {
;     const char* kb = Kslot + hi * 1024 + r32 * 16;
; #pragma unroll
;     for (int d0 = 0; d0 < 4; ++d0) {
;         const s16x8 b0 = *reinterpret_cast<const s16x8*>(kb + d0 * 2048);
;         const s16x8 b1 = *reinterpret_cast<const s16x8*>(kb + d0 * 2048 + 512);
;         if (d0 == 0) { p0 = MFMA32(b0, qr[0], negm); p1 = MFMA32(b1, qr[0], negm); }
;         else { p0 = MFMA32(b0, qr[d0], p0); p1 = MFMA32(b1, qr[d0], p1); } }
; }
; __device__ __forceinline__ void kload8(s16x8* kf, lds_cptr kp) {
;     kf[0] = LDS8(kp); kf[1] = LDS8(kp + 512); kf[2] = LDS8(kp + 2048); kf[3] = LDS8(kp + 2560);
;     kf[4] = LDS8(kp + 4096); kf[5] = LDS8(kp + 4608); kf[6] = LDS8(kp + 6144); kf[7] = LDS8(kp + 6656);
; }
; template <bool MOBA, int THRL> ...
;     ...
;     { const f32x16 z16 = f32x16{}; qkt(pA0, pA1, Kbase, qr, z16, r32, hi); } asm volatile("s_nop 15\n\ts_nop 7" : "+v"(pA0), "+v"(pA1)); ADDB(pA0, pA1, 0); CMASK(pA0, pA1, 0);
;     START(pA0, pA1);
.LBB0_475:
	v_lshlrev_b32_e32 v0, 10, v32
	v_lshlrev_b32_e32 v1, 4, v227
	v_add3_u32 v232, 0, v0, v1
	v_lshlrev_b32_e32 v0, 1, v98
	v_and_b32_e32 v0, 32, v0
	v_lshlrev_b32_e32 v2, 4, v98
	v_add3_u32 v0, 0, v0, v16
	v_lshlrev_b32_e32 v1, 8, v32
	v_and_b32_e32 v2, 0xc0, v2
	v_add3_u32 v230, v0, v1, v2
	ds_read_b128 v[0:3], v232 offset:512
	ds_read_b128 v[4:7], v232
	s_waitcnt vmcnt(0) lgkmcnt(0)
	v_mfma_f32_32x32x16_f16 v[16:31], v[4:7], v[128:131], 0
	ds_read_b128 v[34:37], v232 offset:2560
	ds_read_b128 v[38:41], v232 offset:2048
	s_and_b32 s0, s18, 0x3fffffc0
	s_lshl_b32 s0, s0, 2
	s_lshl_b32 s26, s11, 10
	s_add_i32 s18, s0, 0
	s_add_i32 s0, s33, s26
	v_add_u32_e32 v33, s0, v214
	v_mfma_f32_32x32x16_f16 v[0:15], v[0:3], v[128:131], 0
	v_or_b32_e32 v215, s2, v227
	v_lshlrev_b32_e32 v233, 2, v32
	v_cmp_le_i32_e32 vcc, v233, v215
	v_or_b32_e32 v32, 51, v233
	s_lshr_b32 s37, s19, 6
	s_mov_b32 s19, 1
	s_mov_b32 s68, 0
	s_waitcnt lgkmcnt(0)
	v_mfma_f32_32x32x16_f16 v[16:31], v[38:41], v[124:127], v[16:31]
	v_add_u32_e32 v234, s33, v214
	v_cmp_gt_u32_e64 s[38:39], 32, v226
	v_lshl_add_u32 v229, v227, 2, s18
	v_lshl_add_u32 v228, v233, 2, s18
	v_mfma_f32_32x32x16_f16 v[0:15], v[34:37], v[124:127], v[0:15]
	ds_read_b128 v[34:37], v232 offset:4608
	ds_read_b128 v[38:41], v232 offset:4096
	s_waitcnt lgkmcnt(0)
	v_mfma_f32_32x32x16_f16 v[16:31], v[38:41], v[120:123], v[16:31]
	v_mfma_f32_32x32x16_f16 v[0:15], v[34:37], v[120:123], v[0:15]
	ds_read_b128 v[34:37], v232 offset:6656
	ds_read_b128 v[38:41], v232 offset:6144
	s_waitcnt lgkmcnt(0)
	v_mfma_f32_32x32x16_f16 v[16:31], v[38:41], v[116:119], v[16:31]
	v_mfma_f32_32x32x16_f16 v[0:15], v[34:37], v[116:119], v[0:15]
	s_nop 15
	s_nop 7
	ds_read_b128 v[34:37], v33
	ds_read_b128 v[38:41], v33 offset:32
	ds_read_b128 v[42:45], v33 offset:128
	s_waitcnt lgkmcnt(2)
	s_nop 6
	v_pk_add_f32 v[46:47], v[34:35], v[16:17]
	v_pk_add_f32 v[48:49], v[36:37], v[18:19]
	ds_read_b128 v[16:19], v33 offset:160
	s_waitcnt lgkmcnt(2)
	v_pk_add_f32 v[38:39], v[20:21], v[38:39]
	v_pk_add_f32 v[40:41], v[22:23], v[40:41]
	ds_read_b128 v[20:23], v33 offset:64
	ds_read_b128 v[34:37], v33 offset:192
	s_waitcnt lgkmcnt(3)
	v_pk_add_f32 v[0:1], v[0:1], v[42:43]
	s_waitcnt lgkmcnt(2)
	v_pk_add_f32 v[4:5], v[4:5], v[16:17]
	v_pk_add_f32 v[6:7], v[6:7], v[18:19]
	s_waitcnt lgkmcnt(1)
	v_pk_add_f32 v[50:51], v[24:25], v[20:21]
	v_pk_add_f32 v[52:53], v[26:27], v[22:23]
	ds_read_b128 v[20:23], v33 offset:96
	ds_read_b128 v[24:27], v33 offset:224
	v_or_b32_e32 v16, 32, v233
	v_or_b32_e32 v18, 33, v233
	v_cmp_le_i32_e64 s[0:1], v16, v215
	v_cndmask_b32_e32 v16, v248, v46, vcc
	v_cmp_le_i32_e32 vcc, v18, v215
	v_or_b32_e32 v18, 2, v233
	v_or_b32_e32 v19, 34, v233
	v_cndmask_b32_e32 v1, v248, v1, vcc
	v_cmp_le_i32_e32 vcc, v18, v215
	v_pk_add_f32 v[2:3], v[2:3], v[44:45]
	s_waitcnt lgkmcnt(0)
	v_pk_add_f32 v[12:13], v[12:13], v[24:25]
	v_cndmask_b32_e32 v18, v248, v48, vcc
	v_cmp_le_i32_e32 vcc, v19, v215
	v_or_b32_e32 v19, 3, v233
	v_or_b32_e32 v24, 35, v233
	v_cndmask_b32_e32 v2, v248, v2, vcc
	v_cmp_le_i32_e32 vcc, v19, v215
	v_or_b32_e32 v25, 40, v233
	v_pk_add_f32 v[14:15], v[14:15], v[26:27]
	v_cndmask_b32_e32 v19, v248, v49, vcc
	v_cmp_le_i32_e32 vcc, v24, v215
	v_or_b32_e32 v24, 8, v233
	v_or_b32_e32 v26, 41, v233
	v_cndmask_b32_e32 v3, v248, v3, vcc
	v_cmp_le_i32_e32 vcc, v24, v215
	v_or_b32_e32 v27, 42, v233
	v_pk_add_f32 v[20:21], v[28:29], v[20:21]
	v_cndmask_b32_e32 v24, v248, v38, vcc
	v_cmp_le_i32_e32 vcc, v25, v215
	v_or_b32_e32 v25, 9, v233
	v_or_b32_e32 v28, 43, v233
	v_cndmask_b32_e32 v4, v248, v4, vcc
	v_cmp_le_i32_e32 vcc, v25, v215
	v_or_b32_e32 v29, 48, v233
	v_pk_add_f32 v[8:9], v[8:9], v[34:35]
	v_cndmask_b32_e32 v25, v248, v39, vcc
	v_cmp_le_i32_e32 vcc, v26, v215
	v_or_b32_e32 v26, 10, v233
	v_pk_add_f32 v[22:23], v[30:31], v[22:23]
	v_cndmask_b32_e32 v5, v248, v5, vcc
	v_cmp_le_i32_e32 vcc, v26, v215
	v_or_b32_e32 v30, 49, v233
	v_or_b32_e32 v31, 50, v233
	v_cndmask_b32_e32 v26, v248, v40, vcc
	v_cmp_le_i32_e32 vcc, v27, v215
	v_or_b32_e32 v27, 11, v233
	v_pk_add_f32 v[10:11], v[10:11], v[36:37]
	v_cndmask_b32_e32 v6, v248, v6, vcc
	v_cmp_le_i32_e32 vcc, v27, v215
	v_cndmask_b32_e64 v0, v248, v0, s[0:1]
	v_cmp_lt_i32_e64 s[0:1], v233, v215
	v_cndmask_b32_e32 v27, v248, v41, vcc
	v_cmp_le_i32_e32 vcc, v28, v215
	v_or_b32_e32 v28, 16, v233
	v_cndmask_b32_e64 v17, v248, v47, s[0:1]
	v_cndmask_b32_e32 v7, v248, v7, vcc
	v_cmp_le_i32_e32 vcc, v28, v215
	v_max3_f32 v33, v18, v19, v1
	s_add_i32 s0, s26, 0
	v_max3_f32 v33, v33, v26, v27
	s_lshl_b32 s26, s11, 2
	v_cndmask_b32_e32 v28, v248, v50, vcc
	v_cmp_le_i32_e32 vcc, v29, v215
	v_or_b32_e32 v29, 17, v233
	v_max3_f32 v33, v33, v6, v7
	s_cmp_lg_u32 0, -1
	v_cndmask_b32_e32 v8, v248, v8, vcc
	v_cmp_le_i32_e32 vcc, v29, v215
	s_nop 1
	v_cndmask_b32_e32 v29, v248, v51, vcc
	v_cmp_le_i32_e32 vcc, v30, v215
	v_or_b32_e32 v30, 18, v233
	s_nop 0
	v_cndmask_b32_e32 v9, v248, v9, vcc
	v_cmp_le_i32_e32 vcc, v30, v215
	s_nop 1
	v_cndmask_b32_e32 v30, v248, v52, vcc
	v_cmp_le_i32_e32 vcc, v31, v215
	v_or_b32_e32 v31, 19, v233
	s_nop 0
	v_cndmask_b32_e32 v10, v248, v10, vcc
	v_cmp_le_i32_e32 vcc, v31, v215
	s_nop 1
	v_cndmask_b32_e32 v31, v248, v53, vcc
	v_cmp_le_i32_e32 vcc, v32, v215
	v_or_b32_e32 v32, 24, v233
	v_max3_f32 v33, v33, v30, v31
	s_nop 0
	v_cndmask_b32_e32 v11, v248, v11, vcc
	v_cmp_le_i32_e32 vcc, v32, v215
	v_or_b32_e32 v32, 56, v233
	v_max3_f32 v33, v33, v10, v11
	s_nop 0
	v_cndmask_b32_e32 v20, v248, v20, vcc
	v_cmp_le_i32_e32 vcc, v32, v215
	v_or_b32_e32 v32, 25, v233
	s_nop 0
	v_cndmask_b32_e32 v12, v248, v12, vcc
	v_cmp_le_i32_e32 vcc, v32, v215
; #define WAIT_BAR(N) asm volatile("s_waitcnt vmcnt(" #N ") lgkmcnt(0)\n\ts_barrier" ::: "memory")
; #define DMA_K(t, slot) glds16(ksrc + (long)AMAP(t) * KVBLK * PQ, (unsigned)__builtin_amdgcn_readfirstlane(kdst + (slot)))
; #define DMA_V(t, slot) glds16(vsrc + (long)AMAP(t) * KVBLK * PQ, (unsigned)__builtin_amdgcn_readfirstlane(vdst + (slot)))
; #define BIASPTR(t) ([&]() -> lds_cptr { const int kt_ = AMAP(t); lds_cptr tb_ = shm3 + LDS_BT + kt_ * 256 + 16 * hi; \
;         if (MOBA) { const bool s_ = ((t) < 4) || ((selbits >> (kt_ >> 2)) & 1u); tb_ = s_ ? tb_ : (shm3 + LDS_INF + 16 * hi); } return tb_; }())
; #define INITLD(P0, P1, bp, g_) do { const f32x4 b0_ = *(lds_cf32x4*)((bp) + 32 * (g_)), b1_ = *(lds_cf32x4*)((bp) + 128 + 32 * (g_)); \
;         _Pragma("unroll") for (int i_ = 0; i_ < 4; ++i_) { P0[4 * (g_) + i_] = b0_[i_]; P1[4 * (g_) + i_] = b1_[i_]; } } while (0)
; #define INITSUB(P, h_) do { _Pragma("unroll") for (int i_ = 0; i_ < 8; ++i_) P[8 * (h_) + i_] -= mhat; asm volatile("" : "+v"(P)); } while (0)
; #define START(P0, P1) do { const float rm = rowmax(P0, P1); resc = false; \
;     { const float dl = rm; mhat = fadd_s(mhat, dl); \
;       _Pragma("unroll") for (int r = 0; r < 16; ++r) { P0[r] = fsub_s(P0[r], dl); P1[r] = fsub_s(P1[r], dl); } } \
;     _Pragma("unroll") for (int r = 0; r < 16; ++r) P0[r] = __builtin_amdgcn_exp2f(P0[r]); } while (0)
; #define ROT() do { sl_prev = sl_cur; sl_cur = sl_next; sl_next = (sl_next == (NSLOT - 1) * SLOTB) ? 0 : sl_next + SLOTB; } while (0)
; template <bool MOBA, int THRL> ...
;     ...
;     bool resc = false;
;     ...
;     START(pA0, pA1);
;     { const lds_cptr bp_ = BIASPTR(1); INITLD(pB0, pB1, bp_, 0); INITLD(pB0, pB1, bp_, 1); INITLD(pB0, pB1, bp_, 2); INITLD(pB0, pB1, bp_, 3);
;       INITSUB(pB0, 0); INITSUB(pB0, 1); INITSUB(pB1, 0); INITSUB(pB1, 1); }
;     _Pragma("unroll") for (int r = 0; r < 16; ++r) pA1[r] = __builtin_amdgcn_exp2f(pA1[r]);
;     WAIT_BAR(0);
;     DMA_K(3, 0); DMA_V(1, SLOTB);
;     ROT();
;     kload8(kf, kp0 + sl_cur);
;     WAIT_BAR(2);
	v_or_b32_e32 v32, 57, v233
	s_nop 0
	v_cndmask_b32_e32 v21, v248, v21, vcc
	v_cmp_le_i32_e32 vcc, v32, v215
	v_or_b32_e32 v32, 26, v233
	s_nop 0
	v_cndmask_b32_e32 v13, v248, v13, vcc
	v_cmp_le_i32_e32 vcc, v32, v215
	v_or_b32_e32 v32, 58, v233
	s_nop 0
	v_cndmask_b32_e32 v22, v248, v22, vcc
	v_cmp_le_i32_e32 vcc, v32, v215
	v_or_b32_e32 v32, 27, v233
	s_nop 0
	v_cndmask_b32_e32 v14, v248, v14, vcc
	v_cmp_le_i32_e32 vcc, v32, v215
	v_or_b32_e32 v32, 59, v233
	s_nop 0
	v_cndmask_b32_e32 v23, v248, v23, vcc
	v_cmp_le_i32_e32 vcc, v32, v215
	v_max3_f32 v32, v16, v17, v0
	v_max3_f32 v33, v33, v22, v23
	s_nop 0
	v_max3_f32 v32, v32, v2, v3
	s_nop 0
	v_max3_f32 v32, v32, v24, v25
	v_cndmask_b32_e32 v15, v248, v15, vcc
	v_max3_f32 v32, v32, v4, v5
	v_max3_f32 v33, v33, v14, v15
	s_nop 0
	v_max3_f32 v32, v32, v28, v29
	s_nop 0
	v_max3_f32 v32, v32, v8, v9
	s_nop 0
	v_max3_f32 v32, v32, v20, v21
	s_nop 0
	v_max3_f32 v32, v32, v12, v13
	s_nop 0
	v_max_f32_e32 v32, v32, v33
	s_nop 0
	v_mov_b32_e32 v33, v32
	s_nop 1
	v_permlane32_swap_b32_e32 v32, v33
	v_max_f32_e32 v32, v32, v33
	s_nop 0
	v_sub_f32_e32 v64, v0, v32
	v_sub_f32_e32 v0, v17, v32
	v_sub_f32_e32 v16, v16, v32
	v_sub_f32_e32 v17, v1, v32
	v_sub_f32_e32 v1, v18, v32
	v_sub_f32_e32 v18, v2, v32
	v_sub_f32_e32 v2, v19, v32
	s_nop 0
	v_exp_f32_e32 v81, v0
	v_add_u32_e32 v0, s0, v214
	v_sub_f32_e32 v19, v3, v32
	v_sub_f32_e32 v3, v24, v32
	v_sub_f32_e32 v24, v4, v32
	v_sub_f32_e32 v4, v25, v32
	v_sub_f32_e32 v25, v5, v32
	v_sub_f32_e32 v5, v26, v32
	v_sub_f32_e32 v26, v6, v32
	v_sub_f32_e32 v6, v27, v32
	v_sub_f32_e32 v27, v7, v32
	v_sub_f32_e32 v7, v28, v32
	v_sub_f32_e32 v28, v8, v32
	v_sub_f32_e32 v8, v29, v32
	v_sub_f32_e32 v29, v9, v32
	v_sub_f32_e32 v9, v30, v32
	v_sub_f32_e32 v30, v10, v32
	v_sub_f32_e32 v10, v31, v32
	v_sub_f32_e32 v31, v11, v32
	v_sub_f32_e32 v11, v20, v32
	v_sub_f32_e32 v20, v12, v32
	v_sub_f32_e32 v12, v21, v32
	v_sub_f32_e32 v21, v13, v32
	v_sub_f32_e32 v13, v22, v32
	v_sub_f32_e32 v22, v14, v32
	v_sub_f32_e32 v14, v23, v32
	v_exp_f32_e32 v80, v16
	v_add_u32_e32 v16, 0x14900, v0
	v_sub_f32_e32 v23, v15, v32
	v_exp_f32_e32 v82, v1
	v_exp_f32_e32 v83, v2
	v_exp_f32_e32 v84, v3
	v_exp_f32_e32 v85, v4
	v_exp_f32_e32 v86, v5
	v_exp_f32_e32 v87, v6
	v_exp_f32_e32 v88, v7
	v_exp_f32_e32 v89, v8
	v_exp_f32_e32 v90, v9
	v_exp_f32_e32 v91, v10
	v_exp_f32_e32 v92, v11
	v_exp_f32_e32 v93, v12
	v_exp_f32_e32 v94, v13
	v_exp_f32_e32 v95, v14
	ds_read_b128 v[0:3], v16
	ds_read_b128 v[4:7], v16 offset:32
	ds_read_b128 v[8:11], v16 offset:128
	ds_read_b128 v[12:15], v16 offset:160
	ds_read_b128 v[56:59], v16 offset:64
	ds_read_b128 v[40:43], v16 offset:192
	ds_read_b128 v[60:63], v16 offset:96
	ds_read_b128 v[44:47], v16 offset:224
	v_add_f32_e32 v218, v97, v32
	s_mov_b64 s[0:1], 0x2a0000
	s_waitcnt lgkmcnt(7)
	v_sub_f32_e32 v48, v0, v218
	v_sub_f32_e32 v49, v1, v218
	v_sub_f32_e32 v50, v2, v218
	v_sub_f32_e32 v51, v3, v218
	s_waitcnt lgkmcnt(6)
	v_sub_f32_e32 v52, v4, v218
	v_sub_f32_e32 v53, v5, v218
	v_sub_f32_e32 v54, v6, v218
	v_sub_f32_e32 v55, v7, v218
	s_waitcnt lgkmcnt(5)
	v_sub_f32_e32 v32, v8, v218
	v_sub_f32_e32 v33, v9, v218
	s_waitcnt lgkmcnt(1)
	v_sub_f32_e32 v34, v10, v218
	v_sub_f32_e32 v35, v11, v218
	v_sub_f32_e32 v56, v56, v218
	v_sub_f32_e32 v57, v57, v218
	v_sub_f32_e32 v58, v58, v218
	v_sub_f32_e32 v59, v59, v218
	v_sub_f32_e32 v60, v60, v218
	v_sub_f32_e32 v61, v61, v218
	v_sub_f32_e32 v62, v62, v218
	v_sub_f32_e32 v63, v63, v218
	v_sub_f32_e32 v36, v12, v218
	v_sub_f32_e32 v37, v13, v218
	v_sub_f32_e32 v38, v14, v218
	v_sub_f32_e32 v39, v15, v218
	v_lshl_add_u64 v[0:1], v[134:135], 0, s[0:1]
	s_waitcnt lgkmcnt(0)
	v_exp_f32_e32 v64, v64
	v_sub_f32_e32 v40, v40, v218
	v_sub_f32_e32 v41, v41, v218
	v_sub_f32_e32 v42, v42, v218
	v_sub_f32_e32 v43, v43, v218
	v_sub_f32_e32 v44, v44, v218
	v_sub_f32_e32 v45, v45, v218
	v_sub_f32_e32 v46, v46, v218
	v_sub_f32_e32 v47, v47, v218
	v_exp_f32_e32 v65, v17
	s_waitcnt vmcnt(0) lgkmcnt(0)
	s_barrier
	s_mov_b32 s0, m0
	s_mov_b32 m0, s89
	s_nop 0
	global_load_lds_dwordx4 v[0:1], off
	s_mov_b32 m0, s0
	s_cselect_b32 s0, 0, 0
	s_add_i32 s0, s0, s90
	v_lshl_add_u64 v[0:1], v[132:133], 0, s[30:31]
	s_add_i32 s0, s0, 0x8000
	s_mov_b32 s1, m0
	s_mov_b32 m0, s0
	s_nop 0
	global_load_lds_dwordx4 v[0:1], off
	s_mov_b32 m0, s1
	ds_read_b128 v[176:179], v232 offset:8192
	ds_read_b128 v[172:175], v232 offset:8704
	ds_read_b128 v[168:171], v232 offset:10240
	ds_read_b128 v[164:167], v232 offset:10752
	ds_read_b128 v[160:163], v232 offset:12288
	ds_read_b128 v[152:155], v232 offset:12800
	ds_read_b128 v[156:159], v232 offset:14336
	ds_read_b128 v[148:151], v232 offset:14848
	v_exp_f32_e32 v66, v18
	v_exp_f32_e32 v67, v19
	v_exp_f32_e32 v68, v24
	v_exp_f32_e32 v69, v25
	v_exp_f32_e32 v70, v26
	v_exp_f32_e32 v71, v27
	v_exp_f32_e32 v72, v28
	v_exp_f32_e32 v73, v29
	v_exp_f32_e32 v74, v30
	v_exp_f32_e32 v75, v31
	v_exp_f32_e32 v76, v20
	v_exp_f32_e32 v77, v21
	v_exp_f32_e32 v78, v22
	v_exp_f32_e32 v79, v23
	s_waitcnt vmcnt(2) lgkmcnt(0)
	s_barrier
	s_cmp_eq_u32 s11, 0
	s_cselect_b64 s[42:43], -1, 0
	s_and_b64 vcc, exec, s[42:43]
	s_cbranch_vccnz .LBB0_495
	v_mov_b32_e32 v16, v97
	v_mov_b32_e32 v17, v97
	s_add_i32 s0, 0, 0x16800
	v_mov_b32_e32 v18, v97
	v_mov_b32_e32 v19, v97
	v_mov_b32_e32 v20, v97
	v_mov_b32_e32 v21, v97
	v_mov_b32_e32 v22, v97
	v_mov_b32_e32 v23, v97
	v_mov_b32_e32 v24, v97
	v_mov_b32_e32 v25, v97
	v_mov_b32_e32 v26, v97
	v_mov_b32_e32 v27, v97
	v_mov_b32_e32 v28, v97
	v_mov_b32_e32 v29, v97
	v_mov_b32_e32 v30, v97
	v_mov_b32_e32 v31, v97
	v_mov_b64_e32 v[0:1], v[16:17]
	s_mov_b32 s69, 1
	s_or_b32 s50, s26, 1
	v_add_u32_e32 v196, s0, v214
	s_or_b32 s51, s26, 2
	v_add_u32_e32 v197, 0xbb, v233
	s_mov_b32 s0, 0
	s_movk_i32 s68, 0x4000
	s_movk_i32 s70, 0x2000
	v_mov_b32_e32 v235, 0
	v_mov_b64_e32 v[194:195], v[192:193]
	v_mov_b64_e32 v[2:3], v[18:19]
	v_mov_b64_e32 v[4:5], v[20:21]
	v_mov_b64_e32 v[6:7], v[22:23]
	v_mov_b64_e32 v[8:9], v[24:25]
	v_mov_b64_e32 v[10:11], v[26:27]
	v_mov_b64_e32 v[12:13], v[28:29]
	v_mov_b64_e32 v[14:15], v[30:31]

; #define WAIT_BAR(N) asm volatile("s_waitcnt vmcnt(" #N ") lgkmcnt(0)\n\ts_barrier" ::: "memory")
; #define RESC() do { if (resc) { asm volatile("s_waitcnt lgkmcnt(0)" ::: "memory"); \
;       _Pragma("unroll") for (int d_ = 0; d_ < 2; ++d_) _Pragma("unroll") for (int r = 0; r < 16; ++r) o[d_][r] *= wsf[crow(r, hi)]; } } while (0)
; #define ROT() do { sl_prev = sl_cur; sl_cur = sl_next; sl_next = (sl_next == (NSLOT - 1) * SLOTB) ? 0 : sl_next + SLOTB; } while (0)
; template <bool MOBA, int THRL> ...
;     ...
;     int t = 1;
;     ...
;     for (; t + 5 < NT; t += 2) {
;         STEP(pB0, pB1, pA0, pA1, t, true, true, true);       WAIT_BAR(2); RESC(); ROT();
.LBB0_480:
	v_lshl_add_u32 v68, s18, 8, v234
	s_ashr_i32 s18, s18, 2
	v_bfe_u32 v69, v231, s18, 1
	v_cmp_eq_u32_e32 vcc, 0, v69
	s_nop 1
	v_cndmask_b32_e32 v69, v68, v196, vcc
	v_cndmask_b32_e64 v76, v69, v68, s[40:41]
	s_waitcnt lgkmcnt(14)
	v_mfma_f32_32x32x16_f16 v[16:31], v[144:147], v[180:183], v[16:31]
	v_exp_f32_e32 v48, v48
	v_exp_f32_e32 v49, v49
	v_exp_f32_e32 v50, v50
	v_exp_f32_e32 v51, v51
	ds_read_b128 v[156:159], v76
	ds_read_b128 v[68:71], v76 offset:128
	s_waitcnt lgkmcnt(14)
	v_mfma_f32_32x32x16_f16 v[0:15], v[144:147], v[176:179], v[0:15]
	v_exp_f32_e32 v52, v52
	v_exp_f32_e32 v53, v53
	v_exp_f32_e32 v54, v54
	v_exp_f32_e32 v55, v55
	ds_read_b128 v[168:171], v76 offset:32
	ds_read_b128 v[200:203], v76 offset:160
	v_add_u32_e32 v144, s68, v232
	ds_read_b128 v[188:191], v144
	ds_read_b128 v[148:151], v144 offset:512
	s_waitcnt lgkmcnt(14)
	v_mfma_f32_32x32x16_f16 v[16:31], v[140:143], v[172:175], v[16:31]
	v_exp_f32_e32 v56, v56
	v_exp_f32_e32 v57, v57
	v_exp_f32_e32 v58, v58
	v_exp_f32_e32 v59, v59
	ds_read_b128 v[88:91], v76 offset:64
	ds_read_b128 v[72:75], v76 offset:192
	ds_read_b128 v[184:187], v144 offset:2048
	ds_read_b128 v[172:175], v144 offset:2560
	v_mfma_f32_32x32x16_f16 v[0:15], v[140:143], v[84:87], v[0:15]
	v_exp_f32_e32 v60, v60
	v_exp_f32_e32 v61, v61
	v_exp_f32_e32 v62, v62
	v_exp_f32_e32 v63, v63
	ds_read_b128 v[92:95], v76 offset:96
	ds_read_b128 v[76:79], v76 offset:224
	ds_read_b128 v[176:179], v144 offset:4096
	ds_read_b128 v[164:167], v144 offset:4608
	s_waitcnt lgkmcnt(14)
	v_mfma_f32_32x32x16_f16 v[16:31], v[136:139], v[80:83], v[16:31]
	v_exp_f32_e32 v32, v32
	v_exp_f32_e32 v33, v33
	v_exp_f32_e32 v34, v34
	v_exp_f32_e32 v35, v35
	s_waitcnt lgkmcnt(13)
	v_sub_f32_e32 v80, v156, v218
	v_sub_f32_e32 v81, v157, v218
	v_sub_f32_e32 v82, v158, v218
	v_sub_f32_e32 v83, v159, v218
	s_waitcnt lgkmcnt(11)
	v_sub_f32_e32 v84, v168, v218
	v_sub_f32_e32 v85, v169, v218
	v_sub_f32_e32 v86, v170, v218
	v_sub_f32_e32 v87, v171, v218
	s_waitcnt lgkmcnt(3)
	ds_read_b128 v[180:183], v144 offset:6144
	ds_read_b128 v[168:171], v144 offset:6656
	v_mfma_f32_32x32x16_f16 v[0:15], v[136:139], v[160:163], v[0:15]
	v_exp_f32_e32 v36, v36
	v_exp_f32_e32 v37, v37
	v_exp_f32_e32 v38, v38
	v_exp_f32_e32 v39, v39
	v_sub_f32_e32 v88, v88, v218
	v_sub_f32_e32 v89, v89, v218
	v_sub_f32_e32 v90, v90, v218
	v_sub_f32_e32 v91, v91, v218
	v_sub_f32_e32 v92, v92, v218
	v_sub_f32_e32 v93, v93, v218
	v_sub_f32_e32 v94, v94, v218
	v_sub_f32_e32 v95, v95, v218
	s_nop 0
	v_mfma_f32_32x32x16_f16 v[16:31], v[132:135], v[64:67], v[16:31]
	v_exp_f32_e32 v40, v40
	v_exp_f32_e32 v41, v41
	v_exp_f32_e32 v42, v42
	v_exp_f32_e32 v43, v43
	v_sub_f32_e32 v64, v68, v218
	v_sub_f32_e32 v65, v69, v218
	v_sub_f32_e32 v66, v70, v218
	v_sub_f32_e32 v67, v71, v218
	v_sub_f32_e32 v68, v200, v218
	v_sub_f32_e32 v69, v201, v218
	v_sub_f32_e32 v70, v202, v218
	v_sub_f32_e32 v71, v203, v218
	s_waitcnt lgkmcnt(4)
	v_mfma_f32_32x32x16_f16 v[0:15], v[132:135], v[152:155], v[0:15]
	v_exp_f32_e32 v44, v44
	v_exp_f32_e32 v45, v45
	v_exp_f32_e32 v46, v46
	v_exp_f32_e32 v47, v47
	v_sub_f32_e32 v72, v72, v218
	v_sub_f32_e32 v73, v73, v218
	v_sub_f32_e32 v74, v74, v218
	v_sub_f32_e32 v75, v75, v218
	v_sub_f32_e32 v76, v76, v218
	v_sub_f32_e32 v77, v77, v218
	v_sub_f32_e32 v78, v78, v218
	v_sub_f32_e32 v79, v79, v218
	s_nop 0
	s_waitcnt vmcnt(2) lgkmcnt(0)
	s_barrier
	s_andn2_b64 vcc, exec, s[0:1]
	s_cbranch_vccnz .LBB0_482
	s_waitcnt lgkmcnt(0)
	ds_read_b128 v[152:155], v228 offset:49248
	ds_read_b128 v[156:159], v228 offset:49216
	ds_read_b128 v[160:163], v228 offset:49184
	ds_read_b128 v[200:203], v228 offset:49152
	s_waitcnt lgkmcnt(3)
	v_pk_mul_f32 v[30:31], v[30:31], v[154:155]
	s_waitcnt lgkmcnt(2)
	v_pk_mul_f32 v[26:27], v[26:27], v[158:159]
	s_waitcnt lgkmcnt(1)
	v_pk_mul_f32 v[22:23], v[22:23], v[162:163]
	s_waitcnt lgkmcnt(0)
	v_pk_mul_f32 v[18:19], v[18:19], v[202:203]
	v_pk_mul_f32 v[28:29], v[28:29], v[152:153]
	v_pk_mul_f32 v[24:25], v[24:25], v[156:157]
	v_pk_mul_f32 v[20:21], v[20:21], v[160:161]
	v_pk_mul_f32 v[16:17], v[16:17], v[200:201]
	v_pk_mul_f32 v[14:15], v[14:15], v[154:155]
	v_pk_mul_f32 v[10:11], v[10:11], v[158:159]
	v_pk_mul_f32 v[6:7], v[6:7], v[162:163]
	v_pk_mul_f32 v[2:3], v[2:3], v[202:203]
	v_pk_mul_f32 v[12:13], v[12:13], v[152:153]
	v_pk_mul_f32 v[8:9], v[8:9], v[156:157]
	v_pk_mul_f32 v[4:5], v[4:5], v[160:161]
	v_pk_mul_f32 v[0:1], v[0:1], v[200:201]

; #define WAIT_BAR(N) asm volatile("s_waitcnt vmcnt(" #N ") lgkmcnt(0)\n\ts_barrier" ::: "memory")
; #define RESC() do { if (resc) { asm volatile("s_waitcnt lgkmcnt(0)" ::: "memory"); \
;       _Pragma("unroll") for (int d_ = 0; d_ < 2; ++d_) _Pragma("unroll") for (int r = 0; r < 16; ++r) o[d_][r] *= wsf[crow(r, hi)]; } } while (0)
; #define ROT() do { sl_prev = sl_cur; sl_cur = sl_next; sl_next = (sl_next == (NSLOT - 1) * SLOTB) ? 0 : sl_next + SLOTB; } while (0)
; template <bool MOBA, int THRL> ...
;     ...
;     int t = 1;
;     ...
;     for (; t + 5 < NT; t += 2) {
;         STEP(pB0, pB1, pA0, pA1, t, true, true, true);       WAIT_BAR(2); RESC(); ROT();
.LBB0_485:
	v_lshl_add_u32 v36, s18, 8, v234
	s_ashr_i32 s18, s18, 2
	v_bfe_u32 v37, v231, s18, 1
	v_cmp_eq_u32_e32 vcc, 0, v37
	s_nop 1
	v_cndmask_b32_e32 v37, v36, v196, vcc
	v_cndmask_b32_e64 v44, v37, v36, s[0:1]
	s_waitcnt lgkmcnt(14)
	v_mfma_f32_32x32x16_f16 v[16:31], v[144:147], v[156:159], v[16:31]
	v_exp_f32_e32 v80, v80
	v_exp_f32_e32 v81, v81
	v_exp_f32_e32 v82, v82
	v_exp_f32_e32 v83, v83
	ds_read_b128 v[156:159], v44
	ds_read_b128 v[36:39], v44 offset:128
	s_waitcnt lgkmcnt(14)
	v_mfma_f32_32x32x16_f16 v[0:15], v[144:147], v[152:155], v[0:15]
	v_exp_f32_e32 v84, v84
	v_exp_f32_e32 v85, v85
	v_exp_f32_e32 v86, v86
	v_exp_f32_e32 v87, v87
	ds_read_b128 v[188:191], v44 offset:32
	ds_read_b128 v[198:201], v44 offset:160
	v_add_u32_e32 v144, s45, v232
	ds_read_b128 v[176:179], v144
	ds_read_b128 v[172:175], v144 offset:512
	s_waitcnt lgkmcnt(14)
	v_mfma_f32_32x32x16_f16 v[16:31], v[140:143], v[148:151], v[16:31]
	v_exp_f32_e32 v88, v88
	v_exp_f32_e32 v89, v89
	v_exp_f32_e32 v90, v90
	v_exp_f32_e32 v91, v91
	ds_read_b128 v[56:59], v44 offset:64
	ds_read_b128 v[40:43], v44 offset:192
	ds_read_b128 v[168:171], v144 offset:2048
	ds_read_b128 v[164:167], v144 offset:2560
	v_mfma_f32_32x32x16_f16 v[0:15], v[140:143], v[52:55], v[0:15]
	v_exp_f32_e32 v92, v92
	v_exp_f32_e32 v93, v93
	v_exp_f32_e32 v94, v94
	v_exp_f32_e32 v95, v95
	ds_read_b128 v[60:63], v44 offset:96
	ds_read_b128 v[44:47], v44 offset:224
	ds_read_b128 v[160:163], v144 offset:4096
	ds_read_b128 v[152:155], v144 offset:4608
	s_waitcnt lgkmcnt(14)
	v_mfma_f32_32x32x16_f16 v[16:31], v[136:139], v[48:51], v[16:31]
	v_exp_f32_e32 v64, v64
	v_exp_f32_e32 v65, v65
	v_exp_f32_e32 v66, v66
	v_exp_f32_e32 v67, v67
	s_waitcnt lgkmcnt(13)
	v_sub_f32_e32 v48, v156, v218
	v_sub_f32_e32 v49, v157, v218
	v_sub_f32_e32 v50, v158, v218
	v_sub_f32_e32 v51, v159, v218
	s_waitcnt lgkmcnt(11)
	v_sub_f32_e32 v52, v188, v218
	v_sub_f32_e32 v53, v189, v218
	v_sub_f32_e32 v54, v190, v218
	v_sub_f32_e32 v55, v191, v218
	s_waitcnt lgkmcnt(3)
	ds_read_b128 v[156:159], v144 offset:6144
	ds_read_b128 v[148:151], v144 offset:6656
	v_mfma_f32_32x32x16_f16 v[0:15], v[136:139], v[184:187], v[0:15]
	v_exp_f32_e32 v68, v68
	v_exp_f32_e32 v69, v69
	v_exp_f32_e32 v70, v70
	v_exp_f32_e32 v71, v71
	v_sub_f32_e32 v56, v56, v218
	v_sub_f32_e32 v57, v57, v218
	v_sub_f32_e32 v58, v58, v218
	v_sub_f32_e32 v59, v59, v218
	v_sub_f32_e32 v60, v60, v218
	v_sub_f32_e32 v61, v61, v218
	v_sub_f32_e32 v62, v62, v218
	v_sub_f32_e32 v63, v63, v218
	s_nop 0
	v_mfma_f32_32x32x16_f16 v[16:31], v[132:135], v[32:35], v[16:31]
	v_exp_f32_e32 v72, v72
	v_exp_f32_e32 v73, v73
	v_exp_f32_e32 v74, v74
	v_exp_f32_e32 v75, v75
	v_sub_f32_e32 v32, v36, v218
	v_sub_f32_e32 v33, v37, v218
	v_sub_f32_e32 v34, v38, v218
	v_sub_f32_e32 v35, v39, v218
	v_sub_f32_e32 v36, v198, v218
	v_sub_f32_e32 v37, v199, v218
	v_sub_f32_e32 v38, v200, v218
	v_sub_f32_e32 v39, v201, v218
	s_waitcnt lgkmcnt(4)
	v_mfma_f32_32x32x16_f16 v[0:15], v[132:135], v[180:183], v[0:15]
	v_exp_f32_e32 v76, v76
	v_exp_f32_e32 v77, v77
	v_exp_f32_e32 v78, v78
	v_exp_f32_e32 v79, v79
	v_sub_f32_e32 v40, v40, v218
	v_sub_f32_e32 v41, v41, v218
	v_sub_f32_e32 v42, v42, v218
	v_sub_f32_e32 v43, v43, v218
	v_sub_f32_e32 v44, v44, v218
	v_sub_f32_e32 v45, v45, v218
	v_sub_f32_e32 v46, v46, v218
	v_sub_f32_e32 v47, v47, v218
	s_nop 0
	s_waitcnt vmcnt(2) lgkmcnt(0)
	s_barrier
	s_andn2_b64 vcc, exec, s[40:41]
	s_cbranch_vccnz .LBB0_487
	s_waitcnt lgkmcnt(0)
	ds_read_b128 v[180:183], v228 offset:49248
	ds_read_b128 v[184:187], v228 offset:49216
	ds_read_b128 v[188:191], v228 offset:49184
	ds_read_b128 v[198:201], v228 offset:49152
	s_waitcnt lgkmcnt(3)
	v_pk_mul_f32 v[30:31], v[30:31], v[182:183]
	s_waitcnt lgkmcnt(2)
	v_pk_mul_f32 v[26:27], v[26:27], v[186:187]
	s_waitcnt lgkmcnt(1)
	v_pk_mul_f32 v[22:23], v[22:23], v[190:191]
	s_waitcnt lgkmcnt(0)
	v_pk_mul_f32 v[18:19], v[18:19], v[200:201]
	v_pk_mul_f32 v[28:29], v[28:29], v[180:181]
	v_pk_mul_f32 v[24:25], v[24:25], v[184:185]
	v_pk_mul_f32 v[20:21], v[20:21], v[188:189]
	v_pk_mul_f32 v[16:17], v[16:17], v[198:199]
	v_pk_mul_f32 v[14:15], v[14:15], v[182:183]
	v_pk_mul_f32 v[10:11], v[10:11], v[186:187]
	v_pk_mul_f32 v[6:7], v[6:7], v[190:191]
	v_pk_mul_f32 v[2:3], v[2:3], v[200:201]
	v_pk_mul_f32 v[12:13], v[12:13], v[180:181]
	v_pk_mul_f32 v[8:9], v[8:9], v[184:185]
	v_pk_mul_f32 v[4:5], v[4:5], v[188:189]
	v_pk_mul_f32 v[0:1], v[0:1], v[198:199]

; #define WAIT_BAR(N) asm volatile("s_waitcnt vmcnt(" #N ") lgkmcnt(0)\n\ts_barrier" ::: "memory")
; #define RESC() do { if (resc) { asm volatile("s_waitcnt lgkmcnt(0)" ::: "memory"); \
;       _Pragma("unroll") for (int d_ = 0; d_ < 2; ++d_) _Pragma("unroll") for (int r = 0; r < 16; ++r) o[d_][r] *= wsf[crow(r, hi)]; } } while (0)
; #define ROT() do { sl_prev = sl_cur; sl_cur = sl_next; sl_next = (sl_next == (NSLOT - 1) * SLOTB) ? 0 : sl_next + SLOTB; } while (0)
; #define ENDW(tt) do { if ((tt) + 3 < NT) { WAIT_BAR(2); } else if ((tt) + 2 < NT) { WAIT_BAR(1); } else { WAIT_BAR(0); } } while (0)
; template <bool MOBA, int THRL> ...
;     ...
;     int t = 1;
;     ...
;     for (; t + 5 < NT; t += 2) {
;         STEP(pB0, pB1, pA0, pA1, t, true, true, true);       WAIT_BAR(2); RESC(); ROT();
;         STEP(pA0, pA1, pB0, pB1, t + 1, true, true, true);   WAIT_BAR(2); RESC(); ROT();
;     }
;     for (; t + 1 < NT; t += 2) {
;         STEP(pB0, pB1, pA0, pA1, t, (t + 3 < NT), (t + 1 < NT), (t + 1 < NT));       ENDW(t);     RESC(); ROT();
;         STEP(pA0, pA1, pB0, pB1, t + 1, (t + 4 < NT), (t + 2 < NT), (t + 2 < NT));   ENDW(t + 1); RESC(); ROT();
.LBB0_503:
	v_lshl_add_u32 v69, v68, 8, v234
	v_ashrrev_i32_e32 v68, 2, v68
	v_bfe_u32 v68, v231, v68, 1
	v_cmp_eq_u32_e32 vcc, 0, v68
	s_nop 1
	v_cndmask_b32_e32 v68, v69, v236, vcc
	v_cndmask_b32_e64 v76, v68, v69, s[40:41]
	s_waitcnt lgkmcnt(14)
	v_mfma_f32_32x32x16_f16 v[16:31], v[144:147], v[192:195], v[16:31]
	v_exp_f32_e32 v48, v48
	v_exp_f32_e32 v49, v49
	v_exp_f32_e32 v50, v50
	v_exp_f32_e32 v51, v51
	ds_read_b128 v[148:151], v76
	ds_read_b128 v[68:71], v76 offset:128
	s_waitcnt lgkmcnt(14)
	v_mfma_f32_32x32x16_f16 v[0:15], v[144:147], v[176:179], v[0:15]
	v_exp_f32_e32 v52, v52
	v_exp_f32_e32 v53, v53
	v_exp_f32_e32 v54, v54
	v_exp_f32_e32 v55, v55
	ds_read_b128 v[156:159], v76 offset:32
	ds_read_b128 v[192:195], v76 offset:160
	v_add_u32_e32 v144, s18, v232
	ds_read_b128 v[176:179], v144
	ds_read_b128 v[172:175], v144 offset:512
	s_waitcnt lgkmcnt(14)
	v_mfma_f32_32x32x16_f16 v[16:31], v[140:143], v[188:191], v[16:31]
	v_exp_f32_e32 v56, v56
	v_exp_f32_e32 v57, v57
	v_exp_f32_e32 v58, v58
	v_exp_f32_e32 v59, v59
	ds_read_b128 v[88:91], v76 offset:64
	ds_read_b128 v[72:75], v76 offset:192
	ds_read_b128 v[168:171], v144 offset:2048
	ds_read_b128 v[164:167], v144 offset:2560
	v_mfma_f32_32x32x16_f16 v[0:15], v[140:143], v[84:87], v[0:15]
	v_exp_f32_e32 v60, v60
	v_exp_f32_e32 v61, v61
	v_exp_f32_e32 v62, v62
	v_exp_f32_e32 v63, v63
	ds_read_b128 v[92:95], v76 offset:96
	ds_read_b128 v[76:79], v76 offset:224
	ds_read_b128 v[160:163], v144 offset:4096
	ds_read_b128 v[152:155], v144 offset:4608
	s_waitcnt lgkmcnt(14)
	v_mfma_f32_32x32x16_f16 v[16:31], v[136:139], v[80:83], v[16:31]
	v_exp_f32_e32 v32, v32
	v_exp_f32_e32 v33, v33
	v_exp_f32_e32 v34, v34
	v_exp_f32_e32 v35, v35
	s_waitcnt lgkmcnt(13)
	v_sub_f32_e32 v80, v148, v218
	v_sub_f32_e32 v81, v149, v218
	v_sub_f32_e32 v82, v150, v218
	v_sub_f32_e32 v83, v151, v218
	s_waitcnt lgkmcnt(11)
	v_sub_f32_e32 v84, v156, v218
	v_sub_f32_e32 v85, v157, v218
	v_sub_f32_e32 v86, v158, v218
	v_sub_f32_e32 v87, v159, v218
	s_waitcnt lgkmcnt(3)
	ds_read_b128 v[156:159], v144 offset:6144
	ds_read_b128 v[148:151], v144 offset:6656
	v_mfma_f32_32x32x16_f16 v[0:15], v[136:139], v[184:187], v[0:15]
	v_exp_f32_e32 v36, v36
	v_exp_f32_e32 v37, v37
	v_exp_f32_e32 v38, v38
	v_exp_f32_e32 v39, v39
	v_sub_f32_e32 v88, v88, v218
	v_sub_f32_e32 v89, v89, v218
	v_sub_f32_e32 v90, v90, v218
	v_sub_f32_e32 v91, v91, v218
	v_sub_f32_e32 v92, v92, v218
	v_sub_f32_e32 v93, v93, v218
	v_sub_f32_e32 v94, v94, v218
	v_sub_f32_e32 v95, v95, v218
	s_nop 0
	v_mfma_f32_32x32x16_f16 v[16:31], v[132:135], v[64:67], v[16:31]
	v_exp_f32_e32 v40, v40
	v_exp_f32_e32 v41, v41
	v_exp_f32_e32 v42, v42
	v_exp_f32_e32 v43, v43
	v_sub_f32_e32 v64, v68, v218
	v_sub_f32_e32 v65, v69, v218
	v_sub_f32_e32 v66, v70, v218
	v_sub_f32_e32 v67, v71, v218
	v_sub_f32_e32 v68, v192, v218
	v_sub_f32_e32 v69, v193, v218
	v_sub_f32_e32 v70, v194, v218
	v_sub_f32_e32 v71, v195, v218
	s_waitcnt lgkmcnt(4)
	v_mfma_f32_32x32x16_f16 v[0:15], v[132:135], v[180:183], v[0:15]
	v_exp_f32_e32 v44, v44
	v_exp_f32_e32 v45, v45
	v_exp_f32_e32 v46, v46
	v_exp_f32_e32 v47, v47
	v_sub_f32_e32 v72, v72, v218
	v_sub_f32_e32 v73, v73, v218
	v_sub_f32_e32 v74, v74, v218
	v_sub_f32_e32 v75, v75, v218
	v_sub_f32_e32 v76, v76, v218
	v_sub_f32_e32 v77, v77, v218
	v_sub_f32_e32 v78, v78, v218
	v_sub_f32_e32 v79, v79, v218
	s_nop 0
	s_mov_b64 s[50:51], -1
	s_and_b64 vcc, exec, s[46:47]
	s_cbranch_vccnz .LBB0_546
	s_andn2_b64 vcc, exec, s[50:51]
	s_cbranch_vccz .LBB0_551

.LBB0_530:
	s_waitcnt lgkmcnt(6)
	v_mfma_f32_32x32x16_f16 v[16:31], v[136:139], v[192:195], v[16:31]
	v_exp_f32_e32 v64, v64
	v_exp_f32_e32 v65, v65
	v_exp_f32_e32 v66, v66
	v_exp_f32_e32 v67, v67
	s_and_b64 vcc, exec, s[40:41]
	s_cbranch_vccnz .LBB0_532
	s_waitcnt lgkmcnt(1)
	v_sub_f32_e32 v49, v49, v218
	v_sub_f32_e32 v48, v48, v218
	v_sub_f32_e32 v50, v50, v218
	v_sub_f32_e32 v51, v51, v218
	v_sub_f32_e32 v52, v52, v218
	v_sub_f32_e32 v53, v53, v218
	v_sub_f32_e32 v54, v54, v218
	v_sub_f32_e32 v55, v55, v218
	s_nop 0

.LBB0_534:
	s_waitcnt lgkmcnt(4)
	v_mfma_f32_32x32x16_f16 v[0:15], v[136:139], v[188:191], v[0:15]
	v_exp_f32_e32 v68, v68
	v_exp_f32_e32 v69, v69
	v_exp_f32_e32 v70, v70
	v_exp_f32_e32 v71, v71
	s_and_b64 vcc, exec, s[40:41]
	s_cbranch_vccnz .LBB0_536
	s_waitcnt lgkmcnt(1)
	v_sub_f32_e32 v56, v56, v218
	v_sub_f32_e32 v57, v57, v218
	v_sub_f32_e32 v58, v58, v218
	v_sub_f32_e32 v59, v59, v218
	v_sub_f32_e32 v60, v60, v218
	v_sub_f32_e32 v61, v61, v218
	v_sub_f32_e32 v62, v62, v218
	v_sub_f32_e32 v63, v63, v218
	s_nop 0
.LBB0_536:
	s_waitcnt lgkmcnt(2)
	v_mfma_f32_32x32x16_f16 v[16:31], v[132:135], v[184:187], v[16:31]
	v_exp_f32_e32 v72, v72
	v_exp_f32_e32 v73, v73
	v_exp_f32_e32 v74, v74
	v_exp_f32_e32 v75, v75
	s_and_b64 vcc, exec, s[40:41]
	s_cbranch_vccnz .LBB0_538
	s_waitcnt lgkmcnt(0)
	v_sub_f32_e32 v33, v33, v218
	v_sub_f32_e32 v32, v32, v218
	v_sub_f32_e32 v34, v34, v218
	v_sub_f32_e32 v35, v35, v218
	v_sub_f32_e32 v36, v36, v218
	v_sub_f32_e32 v37, v37, v218
	v_sub_f32_e32 v38, v38, v218
	v_sub_f32_e32 v39, v39, v218
	s_nop 0
.LBB0_538:
	s_waitcnt lgkmcnt(0)
	v_mfma_f32_32x32x16_f16 v[0:15], v[132:135], v[180:183], v[0:15]
	v_exp_f32_e32 v76, v76
	v_exp_f32_e32 v77, v77
	v_exp_f32_e32 v78, v78
	v_exp_f32_e32 v79, v79
	s_and_b64 vcc, exec, s[40:41]
	s_cbranch_vccnz .LBB0_540
	v_sub_f32_e32 v40, v40, v218
	v_sub_f32_e32 v41, v41, v218
	v_sub_f32_e32 v42, v42, v218
	v_sub_f32_e32 v43, v43, v218
	v_sub_f32_e32 v44, v44, v218
	v_sub_f32_e32 v45, v45, v218
	v_sub_f32_e32 v46, v46, v218
	v_sub_f32_e32 v47, v47, v218
	s_nop 0

; __device__ __forceinline__ void cmask(f32x16& p0, f32x16& p1, int jb, int qrel, int hi) {
;     const float NEG = -INFINITY; int kb = 64 * jb + 4 * hi;
; #pragma unroll
;     for (int r = 0; r < 16; ++r) { int kv = kb + (r & 3) + 8 * (r >> 2); if (kv > qrel) p0[r] = NEG; if (kv + 32 > qrel) p1[r] = NEG; }
; }
; __device__ __forceinline__ void glds16(const void* gsrc, unsigned lds_dst) { unsigned keep;
;     asm volatile("s_mov_b32 %0, m0\n\ts_mov_b32 m0, %2\n\ts_nop 0\n\tglobal_load_lds_dwordx4 %1, off\n\ts_mov_b32 m0, %0" : "=&s"(keep) : "v"(gsrc), "s"(lds_dst) : "memory"); }
; __device__ __forceinline__ float max3f(float a, float b, float c) { float r; asm("v_max3_f32 %0, %1, %2, %3" : "=v"(r) : "v"(a), "v"(b), "v"(c)); return r; }
; __device__ __forceinline__ float max2f(float a, float b) { float r; asm("v_max_f32_e32 %0, %1, %2" : "=v"(r) : "v"(a), "v"(b)); return r; }
; __device__ __forceinline__ float fadd_s(float a, float b) { float r; asm("v_add_f32_e32 %0, %1, %2" : "=v"(r) : "v"(a), "v"(b)); return r; }
; __device__ __forceinline__ float fsub_s(float a, float b) { float r; asm("v_sub_f32_e32 %0, %1, %2" : "=v"(r) : "v"(a), "v"(b)); return r; }
; __device__ __forceinline__ unsigned cvtpk_s(float lo, float hi) { return pg8::cvt_pk_f16(lo, hi); }
; __device__ __forceinline__ void qkt(f32x16& p0, f32x16& p1, const char* Kslot, const s16x8* qr, const f32x16& negm, int r32, int hi) {
;     const char* kb = Kslot + hi * 1024 + r32 * 16;
; #pragma unroll
;     for (int d0 = 0; d0 < 4; ++d0) {
;         const s16x8 b0 = *reinterpret_cast<const s16x8*>(kb + d0 * 2048);
;         const s16x8 b1 = *reinterpret_cast<const s16x8*>(kb + d0 * 2048 + 512);
;         if (d0 == 0) { p0 = MFMA32(b0, qr[0], negm); p1 = MFMA32(b1, qr[0], negm); }
;         else { p0 = MFMA32(b0, qr[d0], p0); p1 = MFMA32(b1, qr[d0], p1); } }
; }
; __device__ __forceinline__ void kload8(s16x8* kf, lds_cptr kp) {
;     kf[0] = LDS8(kp); kf[1] = LDS8(kp + 512); kf[2] = LDS8(kp + 2048); kf[3] = LDS8(kp + 2560);
;     kf[4] = LDS8(kp + 4096); kf[5] = LDS8(kp + 4608); kf[6] = LDS8(kp + 6144); kf[7] = LDS8(kp + 6656);
; }
; template <bool MOBA, int THRL> ...
;     ...
;     { const f32x16 z16 = f32x16{}; qkt(pA0, pA1, Kbase, qr, z16, r32, hi); } asm volatile("s_nop 15\n\ts_nop 7" : "+v"(pA0), "+v"(pA1)); ADDB(pA0, pA1, 0); CMASK(pA0, pA1, 0);
;     START(pA0, pA1);
.LBB0_623:
	v_lshlrev_b32_e32 v0, 10, v32
	v_lshlrev_b32_e32 v1, 4, v99
	v_add3_u32 v230, 0, v0, v1
	v_lshlrev_b32_e32 v0, 1, v98
	v_and_b32_e32 v0, 32, v0
	v_add3_u32 v0, 0, v0, v2
	v_lshlrev_b32_e32 v2, 4, v98
	v_lshlrev_b32_e32 v1, 8, v32
	v_and_b32_e32 v2, 0xc0, v2
	v_add3_u32 v229, v0, v1, v2
	ds_read_b128 v[0:3], v230 offset:512
	ds_read_b128 v[4:7], v230
	s_waitcnt vmcnt(0) lgkmcnt(0)
	v_mfma_f32_32x32x16_f16 v[16:31], v[4:7], v[128:131], 0
	ds_read_b128 v[34:37], v230 offset:2560
	ds_read_b128 v[38:41], v230 offset:2048
	s_and_b32 s0, s18, 0x3fffffc0
	s_lshr_b32 s36, s19, 6
	s_lshl_b32 s0, s0, 2
	s_lshl_b32 s19, s11, 10
	s_add_i32 s18, s0, 0
	s_add_i32 s0, s33, s19
	v_mfma_f32_32x32x16_f16 v[0:15], v[0:3], v[128:131], 0
	v_add_u32_e32 v33, s0, v214
	v_or_b32_e32 v215, s46, v99
	v_lshlrev_b32_e32 v231, 2, v32
	v_cmp_le_i32_e32 vcc, v231, v215
	v_or_b32_e32 v32, 51, v231
	s_lshl_b32 s26, s11, 2
	s_mov_b32 s37, 1
	s_waitcnt lgkmcnt(0)
	v_mfma_f32_32x32x16_f16 v[16:31], v[38:41], v[124:127], v[16:31]
	s_mov_b32 s68, 0
	v_add_u32_e32 v232, s33, v214
	v_cmp_gt_u32_e64 s[38:39], 32, v226
	v_lshl_add_u32 v228, v99, 2, s18
	v_lshl_add_u32 v227, v231, 2, s18
	v_mfma_f32_32x32x16_f16 v[0:15], v[34:37], v[124:127], v[0:15]
	ds_read_b128 v[34:37], v230 offset:4608
	ds_read_b128 v[38:41], v230 offset:4096
	s_waitcnt lgkmcnt(0)
	v_mfma_f32_32x32x16_f16 v[16:31], v[38:41], v[120:123], v[16:31]
	v_mfma_f32_32x32x16_f16 v[0:15], v[34:37], v[120:123], v[0:15]
	ds_read_b128 v[34:37], v230 offset:6656
	ds_read_b128 v[38:41], v230 offset:6144
	s_waitcnt lgkmcnt(0)
	v_mfma_f32_32x32x16_f16 v[16:31], v[38:41], v[116:119], v[16:31]
	v_mfma_f32_32x32x16_f16 v[0:15], v[34:37], v[116:119], v[0:15]
	s_nop 15
	s_nop 7
	ds_read_b128 v[34:37], v33
	ds_read_b128 v[38:41], v33 offset:32
	ds_read_b128 v[42:45], v33 offset:128
	s_waitcnt lgkmcnt(2)
	s_nop 6
	v_pk_add_f32 v[46:47], v[34:35], v[16:17]
	v_pk_add_f32 v[48:49], v[36:37], v[18:19]
	ds_read_b128 v[16:19], v33 offset:160
	s_waitcnt lgkmcnt(2)
	v_pk_add_f32 v[38:39], v[20:21], v[38:39]
	v_pk_add_f32 v[40:41], v[22:23], v[40:41]
	ds_read_b128 v[20:23], v33 offset:64
	ds_read_b128 v[34:37], v33 offset:192
	s_waitcnt lgkmcnt(3)
	v_pk_add_f32 v[0:1], v[0:1], v[42:43]
	s_waitcnt lgkmcnt(2)
	v_pk_add_f32 v[4:5], v[4:5], v[16:17]
	v_pk_add_f32 v[6:7], v[6:7], v[18:19]
	s_waitcnt lgkmcnt(1)
	v_pk_add_f32 v[50:51], v[24:25], v[20:21]
	v_pk_add_f32 v[52:53], v[26:27], v[22:23]
	ds_read_b128 v[20:23], v33 offset:96
	ds_read_b128 v[24:27], v33 offset:224
	v_or_b32_e32 v16, 32, v231
	v_or_b32_e32 v18, 33, v231
	v_cmp_le_i32_e64 s[0:1], v16, v215
	v_cndmask_b32_e32 v16, v248, v46, vcc
	v_cmp_le_i32_e32 vcc, v18, v215
	v_or_b32_e32 v18, 2, v231
	v_or_b32_e32 v19, 34, v231
	v_cndmask_b32_e32 v1, v248, v1, vcc
	v_cmp_le_i32_e32 vcc, v18, v215
	v_pk_add_f32 v[2:3], v[2:3], v[44:45]
	s_waitcnt lgkmcnt(0)
	v_pk_add_f32 v[12:13], v[12:13], v[24:25]
	v_cndmask_b32_e32 v18, v248, v48, vcc
	v_cmp_le_i32_e32 vcc, v19, v215
	v_or_b32_e32 v19, 3, v231
	v_or_b32_e32 v24, 35, v231
	v_cndmask_b32_e32 v2, v248, v2, vcc
	v_cmp_le_i32_e32 vcc, v19, v215
	v_or_b32_e32 v25, 40, v231
	v_pk_add_f32 v[14:15], v[14:15], v[26:27]
	v_cndmask_b32_e32 v19, v248, v49, vcc
	v_cmp_le_i32_e32 vcc, v24, v215
	v_or_b32_e32 v24, 8, v231
	v_or_b32_e32 v26, 41, v231
	v_cndmask_b32_e32 v3, v248, v3, vcc
	v_cmp_le_i32_e32 vcc, v24, v215
	v_or_b32_e32 v27, 42, v231
	v_pk_add_f32 v[20:21], v[28:29], v[20:21]
	v_cndmask_b32_e32 v24, v248, v38, vcc
	v_cmp_le_i32_e32 vcc, v25, v215
	v_or_b32_e32 v25, 9, v231
	v_or_b32_e32 v28, 43, v231
	v_cndmask_b32_e32 v4, v248, v4, vcc
	v_cmp_le_i32_e32 vcc, v25, v215
	v_or_b32_e32 v29, 48, v231
	v_pk_add_f32 v[8:9], v[8:9], v[34:35]
	v_cndmask_b32_e32 v25, v248, v39, vcc
	v_cmp_le_i32_e32 vcc, v26, v215
	v_or_b32_e32 v26, 10, v231
	v_pk_add_f32 v[22:23], v[30:31], v[22:23]
	v_cndmask_b32_e32 v5, v248, v5, vcc
	v_cmp_le_i32_e32 vcc, v26, v215
	v_or_b32_e32 v30, 49, v231
	v_or_b32_e32 v31, 50, v231
	v_cndmask_b32_e32 v26, v248, v40, vcc
	v_cmp_le_i32_e32 vcc, v27, v215
	v_or_b32_e32 v27, 11, v231
	v_pk_add_f32 v[10:11], v[10:11], v[36:37]
	v_cndmask_b32_e32 v6, v248, v6, vcc
	v_cmp_le_i32_e32 vcc, v27, v215
	v_cndmask_b32_e64 v0, v248, v0, s[0:1]
	v_cmp_lt_i32_e64 s[0:1], v231, v215
	v_cndmask_b32_e32 v27, v248, v41, vcc
	v_cmp_le_i32_e32 vcc, v28, v215
	v_or_b32_e32 v28, 16, v231
	v_cndmask_b32_e64 v17, v248, v47, s[0:1]
	v_cndmask_b32_e32 v7, v248, v7, vcc
	v_cmp_le_i32_e32 vcc, v28, v215
	v_max3_f32 v33, v18, v19, v1
	s_add_i32 s0, s19, 0
	v_max3_f32 v33, v33, v26, v27
	s_mov_b32 s1, s29
	v_cndmask_b32_e32 v28, v248, v50, vcc
	v_cmp_le_i32_e32 vcc, v29, v215
	v_or_b32_e32 v29, 17, v231
	v_max3_f32 v33, v33, v6, v7
	s_nop 0
	v_cndmask_b32_e32 v8, v248, v8, vcc
	v_cmp_le_i32_e32 vcc, v29, v215
	s_nop 1
	v_cndmask_b32_e32 v29, v248, v51, vcc
	v_cmp_le_i32_e32 vcc, v30, v215
	v_or_b32_e32 v30, 18, v231
	s_nop 0
	v_cndmask_b32_e32 v9, v248, v9, vcc
	v_cmp_le_i32_e32 vcc, v30, v215
	s_nop 1
	v_cndmask_b32_e32 v30, v248, v52, vcc
	v_cmp_le_i32_e32 vcc, v31, v215
	v_or_b32_e32 v31, 19, v231
	s_nop 0
	v_cndmask_b32_e32 v10, v248, v10, vcc
	v_cmp_le_i32_e32 vcc, v31, v215
	s_nop 1
	v_cndmask_b32_e32 v31, v248, v53, vcc
	v_cmp_le_i32_e32 vcc, v32, v215
	v_or_b32_e32 v32, 24, v231
	v_max3_f32 v33, v33, v30, v31
	s_nop 0
	v_cndmask_b32_e32 v11, v248, v11, vcc
	v_cmp_le_i32_e32 vcc, v32, v215
	v_or_b32_e32 v32, 56, v231
	v_max3_f32 v33, v33, v10, v11
	s_nop 0
	v_cndmask_b32_e32 v20, v248, v20, vcc
	v_cmp_le_i32_e32 vcc, v32, v215
	v_or_b32_e32 v32, 25, v231
	s_nop 0
	v_cndmask_b32_e32 v12, v248, v12, vcc
	v_cmp_le_i32_e32 vcc, v32, v215
; #define WAIT_BAR(N) asm volatile("s_waitcnt vmcnt(" #N ") lgkmcnt(0)\n\ts_barrier" ::: "memory")
; #define DMA_K(t, slot) glds16(ksrc + (long)AMAP(t) * KVBLK * PQ, (unsigned)__builtin_amdgcn_readfirstlane(kdst + (slot)))
; #define DMA_V(t, slot) glds16(vsrc + (long)AMAP(t) * KVBLK * PQ, (unsigned)__builtin_amdgcn_readfirstlane(vdst + (slot)))
; #define BIASPTR(t) ([&]() -> lds_cptr { const int kt_ = AMAP(t); lds_cptr tb_ = shm3 + LDS_BT + kt_ * 256 + 16 * hi; \
;         if (MOBA) { const bool s_ = ((t) < 4) || ((selbits >> (kt_ >> 2)) & 1u); tb_ = s_ ? tb_ : (shm3 + LDS_INF + 16 * hi); } return tb_; }())
; #define INITLD(P0, P1, bp, g_) do { const f32x4 b0_ = *(lds_cf32x4*)((bp) + 32 * (g_)), b1_ = *(lds_cf32x4*)((bp) + 128 + 32 * (g_)); \
;         _Pragma("unroll") for (int i_ = 0; i_ < 4; ++i_) { P0[4 * (g_) + i_] = b0_[i_]; P1[4 * (g_) + i_] = b1_[i_]; } } while (0)
; #define INITSUB(P, h_) do { _Pragma("unroll") for (int i_ = 0; i_ < 8; ++i_) P[8 * (h_) + i_] -= mhat; asm volatile("" : "+v"(P)); } while (0)
; #define START(P0, P1) do { const float rm = rowmax(P0, P1); resc = false; \
;     { const float dl = rm; mhat = fadd_s(mhat, dl); \
;       _Pragma("unroll") for (int r = 0; r < 16; ++r) { P0[r] = fsub_s(P0[r], dl); P1[r] = fsub_s(P1[r], dl); } } \
;     _Pragma("unroll") for (int r = 0; r < 16; ++r) P0[r] = __builtin_amdgcn_exp2f(P0[r]); } while (0)
; #define ROT() do { sl_prev = sl_cur; sl_cur = sl_next; sl_next = (sl_next == (NSLOT - 1) * SLOTB) ? 0 : sl_next + SLOTB; } while (0)
; template <bool MOBA, int THRL> ...
;     ...
;     bool resc = false;
;     ...
;     START(pA0, pA1);
;     { const lds_cptr bp_ = BIASPTR(1); INITLD(pB0, pB1, bp_, 0); INITLD(pB0, pB1, bp_, 1); INITLD(pB0, pB1, bp_, 2); INITLD(pB0, pB1, bp_, 3);
;       INITSUB(pB0, 0); INITSUB(pB0, 1); INITSUB(pB1, 0); INITSUB(pB1, 1); }
;     _Pragma("unroll") for (int r = 0; r < 16; ++r) pA1[r] = __builtin_amdgcn_exp2f(pA1[r]);
;     WAIT_BAR(0);
;     DMA_K(3, 0); DMA_V(1, SLOTB);
;     ROT();
;     kload8(kf, kp0 + sl_cur);
;     WAIT_BAR(2);
	v_or_b32_e32 v32, 57, v231
	s_nop 0
	v_cndmask_b32_e32 v21, v248, v21, vcc
	v_cmp_le_i32_e32 vcc, v32, v215
	v_or_b32_e32 v32, 26, v231
	s_nop 0
	v_cndmask_b32_e32 v13, v248, v13, vcc
	v_cmp_le_i32_e32 vcc, v32, v215
	v_or_b32_e32 v32, 58, v231
	s_nop 0
	v_cndmask_b32_e32 v22, v248, v22, vcc
	v_cmp_le_i32_e32 vcc, v32, v215
	v_or_b32_e32 v32, 27, v231
	s_nop 0
	v_cndmask_b32_e32 v14, v248, v14, vcc
	v_cmp_le_i32_e32 vcc, v32, v215
	v_or_b32_e32 v32, 59, v231
	s_nop 0
	v_cndmask_b32_e32 v23, v248, v23, vcc
	v_cmp_le_i32_e32 vcc, v32, v215
	v_max3_f32 v32, v16, v17, v0
	v_max3_f32 v33, v33, v22, v23
	s_nop 0
	v_max3_f32 v32, v32, v2, v3
	s_nop 0
	v_max3_f32 v32, v32, v24, v25
	v_cndmask_b32_e32 v15, v248, v15, vcc
	v_max3_f32 v32, v32, v4, v5
	v_max3_f32 v33, v33, v14, v15
	s_nop 0
	v_max3_f32 v32, v32, v28, v29
	s_nop 0
	v_max3_f32 v32, v32, v8, v9
	s_nop 0
	v_max3_f32 v32, v32, v20, v21
	s_nop 0
	v_max3_f32 v32, v32, v12, v13
	s_nop 0
	v_max_f32_e32 v32, v32, v33
	s_nop 0
	v_mov_b32_e32 v33, v32
	s_nop 1
	v_permlane32_swap_b32_e32 v32, v33
	v_max_f32_e32 v32, v32, v33
	s_nop 0
	v_sub_f32_e32 v64, v0, v32
	v_sub_f32_e32 v0, v17, v32
	v_sub_f32_e32 v16, v16, v32
	v_sub_f32_e32 v17, v1, v32
	v_sub_f32_e32 v1, v18, v32
	v_sub_f32_e32 v18, v2, v32
	v_sub_f32_e32 v2, v19, v32
	s_nop 0
	v_exp_f32_e32 v81, v0
	v_add_u32_e32 v0, s0, v214
	v_sub_f32_e32 v19, v3, v32
	v_sub_f32_e32 v3, v24, v32
	v_sub_f32_e32 v24, v4, v32
	v_sub_f32_e32 v4, v25, v32
	v_sub_f32_e32 v25, v5, v32
	v_sub_f32_e32 v5, v26, v32
	v_sub_f32_e32 v26, v6, v32
	v_sub_f32_e32 v6, v27, v32
	v_sub_f32_e32 v27, v7, v32
	v_sub_f32_e32 v7, v28, v32
	v_sub_f32_e32 v28, v8, v32
	v_sub_f32_e32 v8, v29, v32
	v_sub_f32_e32 v29, v9, v32
	v_sub_f32_e32 v9, v30, v32
	v_sub_f32_e32 v30, v10, v32
	v_sub_f32_e32 v10, v31, v32
	v_sub_f32_e32 v31, v11, v32
	v_sub_f32_e32 v11, v20, v32
	v_sub_f32_e32 v20, v12, v32
	v_sub_f32_e32 v12, v21, v32
	v_sub_f32_e32 v21, v13, v32
	v_sub_f32_e32 v13, v22, v32
	v_sub_f32_e32 v22, v14, v32
	v_sub_f32_e32 v14, v23, v32
	v_exp_f32_e32 v80, v16
	v_add_u32_e32 v16, 0x14900, v0
	v_sub_f32_e32 v23, v15, v32
	v_exp_f32_e32 v82, v1
	v_exp_f32_e32 v83, v2
	v_exp_f32_e32 v84, v3
	v_exp_f32_e32 v85, v4
	v_exp_f32_e32 v86, v5
	v_exp_f32_e32 v87, v6
	v_exp_f32_e32 v88, v7
	v_exp_f32_e32 v89, v8
	v_exp_f32_e32 v90, v9
	v_exp_f32_e32 v91, v10
	v_exp_f32_e32 v92, v11
	v_exp_f32_e32 v93, v12
	v_exp_f32_e32 v94, v13
	v_exp_f32_e32 v95, v14
	ds_read_b128 v[0:3], v16
	ds_read_b128 v[4:7], v16 offset:32
	ds_read_b128 v[8:11], v16 offset:128
	ds_read_b128 v[12:15], v16 offset:160
	ds_read_b128 v[56:59], v16 offset:64
	ds_read_b128 v[40:43], v16 offset:192
	ds_read_b128 v[60:63], v16 offset:96
	ds_read_b128 v[44:47], v16 offset:224
	v_add_f32_e32 v218, v97, v32
	s_or_b32 s0, s26, 3
	s_waitcnt lgkmcnt(7)
	v_sub_f32_e32 v48, v0, v218
	v_sub_f32_e32 v49, v1, v218
	v_sub_f32_e32 v50, v2, v218
	v_sub_f32_e32 v51, v3, v218
	s_waitcnt lgkmcnt(6)
	v_sub_f32_e32 v52, v4, v218
	v_sub_f32_e32 v53, v5, v218
	v_sub_f32_e32 v54, v6, v218
	v_sub_f32_e32 v55, v7, v218
	s_waitcnt lgkmcnt(5)
	v_sub_f32_e32 v32, v8, v218
	v_sub_f32_e32 v33, v9, v218
	s_waitcnt lgkmcnt(1)
	v_sub_f32_e32 v34, v10, v218
	v_sub_f32_e32 v35, v11, v218
	v_sub_f32_e32 v56, v56, v218
	v_sub_f32_e32 v57, v57, v218
	v_sub_f32_e32 v58, v58, v218
	v_sub_f32_e32 v59, v59, v218
	v_sub_f32_e32 v60, v60, v218
	v_sub_f32_e32 v61, v61, v218
	v_sub_f32_e32 v62, v62, v218
	v_sub_f32_e32 v63, v63, v218
	v_sub_f32_e32 v36, v12, v218
	v_sub_f32_e32 v37, v13, v218
	v_sub_f32_e32 v38, v14, v218
	v_sub_f32_e32 v39, v15, v218
	s_mul_i32 s0, s0, 0xe0000
	s_waitcnt lgkmcnt(0)
	v_lshl_add_u64 v[0:1], v[192:193], 0, s[0:1]
	v_sub_f32_e32 v40, v40, v218
	v_sub_f32_e32 v41, v41, v218
	v_sub_f32_e32 v42, v42, v218
	v_sub_f32_e32 v43, v43, v218
	v_sub_f32_e32 v44, v44, v218
	v_sub_f32_e32 v45, v45, v218
	v_sub_f32_e32 v46, v46, v218
	v_sub_f32_e32 v47, v47, v218
	s_cmp_lg_u32 0, -1
	s_waitcnt vmcnt(0) lgkmcnt(0)
	s_barrier
	s_mov_b32 s0, m0
	s_mov_b32 m0, s90
	s_nop 0
	global_load_lds_dwordx4 v[0:1], off
	s_mov_b32 m0, s0
	s_cselect_b32 s0, 0, 0
	s_add_i32 s0, s0, s89
	v_lshl_add_u64 v[0:1], v[132:133], 0, s[30:31]
	s_add_i32 s0, s0, 0x8000
	s_mov_b32 s1, m0
	s_mov_b32 m0, s0
	s_nop 0
	global_load_lds_dwordx4 v[0:1], off
	s_mov_b32 m0, s1
	ds_read_b128 v[176:179], v230 offset:8192
	ds_read_b128 v[172:175], v230 offset:8704
	ds_read_b128 v[168:171], v230 offset:10240
	ds_read_b128 v[164:167], v230 offset:10752
	ds_read_b128 v[160:163], v230 offset:12288
	ds_read_b128 v[152:155], v230 offset:12800
	ds_read_b128 v[156:159], v230 offset:14336
	ds_read_b128 v[148:151], v230 offset:14848
	v_exp_f32_e32 v64, v64
	v_exp_f32_e32 v65, v17
	v_exp_f32_e32 v66, v18
	v_exp_f32_e32 v67, v19
	v_exp_f32_e32 v68, v24
	v_exp_f32_e32 v69, v25
	v_exp_f32_e32 v70, v26
	v_exp_f32_e32 v71, v27
	v_exp_f32_e32 v72, v28
	v_exp_f32_e32 v73, v29
	v_exp_f32_e32 v74, v30
	v_exp_f32_e32 v75, v31
	v_exp_f32_e32 v76, v20
	v_exp_f32_e32 v77, v21
	v_exp_f32_e32 v78, v22
	v_exp_f32_e32 v79, v23
	s_waitcnt vmcnt(2) lgkmcnt(0)
	s_barrier
	s_cmp_eq_u32 s11, 0
	s_cselect_b64 s[0:1], -1, 0
	s_and_b64 vcc, exec, s[0:1]
	s_cbranch_vccnz .LBB0_643
	v_mov_b32_e32 v0, 0x380000
	v_mad_u64_u32 v[0:1], s[18:19], s11, v0, v[192:193]
	v_mov_b32_e32 v16, v97
	v_mov_b32_e32 v17, v97
	v_lshl_add_u64 v[194:195], v[0:1], 0, s[24:25]
	v_mov_b32_e32 v18, v97
	v_mov_b32_e32 v19, v97
	v_mov_b32_e32 v20, v97
	v_mov_b32_e32 v21, v97
	v_mov_b32_e32 v22, v97
	v_mov_b32_e32 v23, v97
	v_mov_b32_e32 v24, v97
	v_mov_b32_e32 v25, v97
	v_mov_b32_e32 v26, v97
	v_mov_b32_e32 v27, v97
	v_mov_b32_e32 v28, v97
	v_mov_b32_e32 v29, v97
	v_mov_b32_e32 v30, v97
	v_mov_b32_e32 v31, v97
	v_mov_b64_e32 v[0:1], v[16:17]
	v_or_b32_e32 v196, 0x60, v231
	s_mov_b32 s19, 0
	s_mov_b32 s45, 1
	s_movk_i32 s68, 0x4000
	s_movk_i32 s69, 0x2000
	v_mov_b32_e32 v233, 0
	v_mov_b64_e32 v[2:3], v[18:19]
	v_mov_b64_e32 v[4:5], v[20:21]
	v_mov_b64_e32 v[6:7], v[22:23]
	v_mov_b64_e32 v[8:9], v[24:25]
	v_mov_b64_e32 v[10:11], v[26:27]
	v_mov_b64_e32 v[12:13], v[28:29]
	v_mov_b64_e32 v[14:15], v[30:31]
	s_mov_b32 s40, 0

; #define WAIT_BAR(N) asm volatile("s_waitcnt vmcnt(" #N ") lgkmcnt(0)\n\ts_barrier" ::: "memory")
; #define RESC() do { if (resc) { asm volatile("s_waitcnt lgkmcnt(0)" ::: "memory"); \
;       _Pragma("unroll") for (int d_ = 0; d_ < 2; ++d_) _Pragma("unroll") for (int r = 0; r < 16; ++r) o[d_][r] *= wsf[crow(r, hi)]; } } while (0)
; #define ROT() do { sl_prev = sl_cur; sl_cur = sl_next; sl_next = (sl_next == (NSLOT - 1) * SLOTB) ? 0 : sl_next + SLOTB; } while (0)
; template <bool MOBA, int THRL> ...
;     ...
;     int t = 1;
;     ...
;     for (; t + 5 < NT; t += 2) {
;         STEP(pB0, pB1, pA0, pA1, t, true, true, true);       WAIT_BAR(2); RESC(); ROT();
.LBB0_628:
	s_waitcnt lgkmcnt(14)
	v_mfma_f32_32x32x16_f16 v[16:31], v[144:147], v[180:183], v[16:31]
	v_exp_f32_e32 v48, v48
	v_exp_f32_e32 v49, v49
	v_exp_f32_e32 v50, v50
	v_exp_f32_e32 v51, v51
	v_lshl_add_u32 v76, s11, 8, v232
	ds_read_b128 v[156:159], v76
	ds_read_b128 v[68:71], v76 offset:128
	s_waitcnt lgkmcnt(14)
	v_mfma_f32_32x32x16_f16 v[0:15], v[144:147], v[176:179], v[0:15]
	v_exp_f32_e32 v52, v52
	v_exp_f32_e32 v53, v53
	v_exp_f32_e32 v54, v54
	v_exp_f32_e32 v55, v55
	ds_read_b128 v[168:171], v76 offset:32
	ds_read_b128 v[198:201], v76 offset:160
	v_add_u32_e32 v144, s68, v230
	ds_read_b128 v[188:191], v144
	ds_read_b128 v[148:151], v144 offset:512
	s_waitcnt lgkmcnt(14)
	v_mfma_f32_32x32x16_f16 v[16:31], v[140:143], v[172:175], v[16:31]
	v_exp_f32_e32 v56, v56
	v_exp_f32_e32 v57, v57
	v_exp_f32_e32 v58, v58
	v_exp_f32_e32 v59, v59
	ds_read_b128 v[88:91], v76 offset:64
	ds_read_b128 v[72:75], v76 offset:192
	ds_read_b128 v[184:187], v144 offset:2048
	ds_read_b128 v[172:175], v144 offset:2560
	v_mfma_f32_32x32x16_f16 v[0:15], v[140:143], v[84:87], v[0:15]
	v_exp_f32_e32 v60, v60
	v_exp_f32_e32 v61, v61
	v_exp_f32_e32 v62, v62
	v_exp_f32_e32 v63, v63
	ds_read_b128 v[92:95], v76 offset:96
	ds_read_b128 v[76:79], v76 offset:224
	ds_read_b128 v[176:179], v144 offset:4096
	ds_read_b128 v[164:167], v144 offset:4608
	s_waitcnt lgkmcnt(14)
	v_mfma_f32_32x32x16_f16 v[16:31], v[136:139], v[80:83], v[16:31]
	v_exp_f32_e32 v32, v32
	v_exp_f32_e32 v33, v33
	v_exp_f32_e32 v34, v34
	v_exp_f32_e32 v35, v35
	s_waitcnt lgkmcnt(13)
	v_sub_f32_e32 v80, v156, v218
	v_sub_f32_e32 v81, v157, v218
	v_sub_f32_e32 v82, v158, v218
	v_sub_f32_e32 v83, v159, v218
	s_waitcnt lgkmcnt(11)
	v_sub_f32_e32 v84, v168, v218
	v_sub_f32_e32 v85, v169, v218
	v_sub_f32_e32 v86, v170, v218
	v_sub_f32_e32 v87, v171, v218
	s_waitcnt lgkmcnt(3)
	ds_read_b128 v[180:183], v144 offset:6144
	ds_read_b128 v[168:171], v144 offset:6656
	v_mfma_f32_32x32x16_f16 v[0:15], v[136:139], v[160:163], v[0:15]
	v_exp_f32_e32 v36, v36
	v_exp_f32_e32 v37, v37
	v_exp_f32_e32 v38, v38
	v_exp_f32_e32 v39, v39
	v_sub_f32_e32 v88, v88, v218
	v_sub_f32_e32 v89, v89, v218
	v_sub_f32_e32 v90, v90, v218
	v_sub_f32_e32 v91, v91, v218
	v_sub_f32_e32 v92, v92, v218
	v_sub_f32_e32 v93, v93, v218
	v_sub_f32_e32 v94, v94, v218
	v_sub_f32_e32 v95, v95, v218
	s_nop 0
	v_mfma_f32_32x32x16_f16 v[16:31], v[132:135], v[64:67], v[16:31]
	v_exp_f32_e32 v40, v40
	v_exp_f32_e32 v41, v41
	v_exp_f32_e32 v42, v42
	v_exp_f32_e32 v43, v43
	v_sub_f32_e32 v64, v68, v218
	v_sub_f32_e32 v65, v69, v218
	v_sub_f32_e32 v66, v70, v218
	v_sub_f32_e32 v67, v71, v218
	v_sub_f32_e32 v68, v198, v218
	v_sub_f32_e32 v69, v199, v218
	v_sub_f32_e32 v70, v200, v218
	v_sub_f32_e32 v71, v201, v218
	s_waitcnt lgkmcnt(4)
	v_mfma_f32_32x32x16_f16 v[0:15], v[132:135], v[152:155], v[0:15]
	v_exp_f32_e32 v44, v44
	v_exp_f32_e32 v45, v45
	v_exp_f32_e32 v46, v46
	v_exp_f32_e32 v47, v47
	v_sub_f32_e32 v72, v72, v218
	v_sub_f32_e32 v73, v73, v218
	v_sub_f32_e32 v74, v74, v218
	v_sub_f32_e32 v75, v75, v218
	v_sub_f32_e32 v76, v76, v218
	v_sub_f32_e32 v77, v77, v218
	v_sub_f32_e32 v78, v78, v218
	v_sub_f32_e32 v79, v79, v218
	s_nop 0
	s_waitcnt vmcnt(2) lgkmcnt(0)
	s_barrier
	s_andn2_b64 vcc, exec, s[50:51]
	s_cbranch_vccnz .LBB0_630
	s_waitcnt lgkmcnt(0)
	ds_read_b128 v[152:155], v227 offset:49248
	ds_read_b128 v[156:159], v227 offset:49216
	ds_read_b128 v[160:163], v227 offset:49184
	ds_read_b128 v[198:201], v227 offset:49152
	s_waitcnt lgkmcnt(3)
	v_pk_mul_f32 v[30:31], v[30:31], v[154:155]
	s_waitcnt lgkmcnt(2)
	v_pk_mul_f32 v[26:27], v[26:27], v[158:159]
	s_waitcnt lgkmcnt(1)
	v_pk_mul_f32 v[22:23], v[22:23], v[162:163]
	s_waitcnt lgkmcnt(0)
	v_pk_mul_f32 v[18:19], v[18:19], v[200:201]
	v_pk_mul_f32 v[28:29], v[28:29], v[152:153]
	v_pk_mul_f32 v[24:25], v[24:25], v[156:157]
	v_pk_mul_f32 v[20:21], v[20:21], v[160:161]
	v_pk_mul_f32 v[16:17], v[16:17], v[198:199]
	v_pk_mul_f32 v[14:15], v[14:15], v[154:155]
	v_pk_mul_f32 v[10:11], v[10:11], v[158:159]
	v_pk_mul_f32 v[6:7], v[6:7], v[162:163]
	v_pk_mul_f32 v[2:3], v[2:3], v[200:201]
	v_pk_mul_f32 v[12:13], v[12:13], v[152:153]
	v_pk_mul_f32 v[8:9], v[8:9], v[156:157]
	v_pk_mul_f32 v[4:5], v[4:5], v[160:161]
	v_pk_mul_f32 v[0:1], v[0:1], v[198:199]

; #define WAIT_BAR(N) asm volatile("s_waitcnt vmcnt(" #N ") lgkmcnt(0)\n\ts_barrier" ::: "memory")
; #define RESC() do { if (resc) { asm volatile("s_waitcnt lgkmcnt(0)" ::: "memory"); \
;       _Pragma("unroll") for (int d_ = 0; d_ < 2; ++d_) _Pragma("unroll") for (int r = 0; r < 16; ++r) o[d_][r] *= wsf[crow(r, hi)]; } } while (0)
; #define ROT() do { sl_prev = sl_cur; sl_cur = sl_next; sl_next = (sl_next == (NSLOT - 1) * SLOTB) ? 0 : sl_next + SLOTB; } while (0)
; template <bool MOBA, int THRL> ...
;     ...
;     int t = 1;
;     ...
;     for (; t + 5 < NT; t += 2) {
;         STEP(pB0, pB1, pA0, pA1, t, true, true, true);       WAIT_BAR(2); RESC(); ROT();
.LBB0_633:
	s_waitcnt lgkmcnt(14)
	v_mfma_f32_32x32x16_f16 v[16:31], v[144:147], v[156:159], v[16:31]
	v_exp_f32_e32 v80, v80
	v_exp_f32_e32 v81, v81
	v_exp_f32_e32 v82, v82
	v_exp_f32_e32 v83, v83
	v_lshl_add_u32 v44, s18, 8, v232
	ds_read_b128 v[156:159], v44
	ds_read_b128 v[36:39], v44 offset:128
	s_waitcnt lgkmcnt(14)
	v_mfma_f32_32x32x16_f16 v[0:15], v[144:147], v[152:155], v[0:15]
	v_exp_f32_e32 v84, v84
	v_exp_f32_e32 v85, v85
	v_exp_f32_e32 v86, v86
	v_exp_f32_e32 v87, v87
	ds_read_b128 v[188:191], v44 offset:32
	ds_read_b128 v[198:201], v44 offset:160
	v_add_u32_e32 v144, s11, v230
	ds_read_b128 v[176:179], v144
	ds_read_b128 v[172:175], v144 offset:512
	s_waitcnt lgkmcnt(14)
	v_mfma_f32_32x32x16_f16 v[16:31], v[140:143], v[148:151], v[16:31]
	v_exp_f32_e32 v88, v88
	v_exp_f32_e32 v89, v89
	v_exp_f32_e32 v90, v90
	v_exp_f32_e32 v91, v91
	ds_read_b128 v[56:59], v44 offset:64
	ds_read_b128 v[40:43], v44 offset:192
	ds_read_b128 v[168:171], v144 offset:2048
	ds_read_b128 v[164:167], v144 offset:2560
	v_mfma_f32_32x32x16_f16 v[0:15], v[140:143], v[52:55], v[0:15]
	v_exp_f32_e32 v92, v92
	v_exp_f32_e32 v93, v93
	v_exp_f32_e32 v94, v94
	v_exp_f32_e32 v95, v95
	ds_read_b128 v[60:63], v44 offset:96
	ds_read_b128 v[44:47], v44 offset:224
	ds_read_b128 v[160:163], v144 offset:4096
	ds_read_b128 v[152:155], v144 offset:4608
	s_waitcnt lgkmcnt(14)
	v_mfma_f32_32x32x16_f16 v[16:31], v[136:139], v[48:51], v[16:31]
	v_exp_f32_e32 v64, v64
	v_exp_f32_e32 v65, v65
	v_exp_f32_e32 v66, v66
	v_exp_f32_e32 v67, v67
	s_waitcnt lgkmcnt(13)
	v_sub_f32_e32 v48, v156, v218
	v_sub_f32_e32 v49, v157, v218
	v_sub_f32_e32 v50, v158, v218
	v_sub_f32_e32 v51, v159, v218
	s_waitcnt lgkmcnt(11)
	v_sub_f32_e32 v52, v188, v218
	v_sub_f32_e32 v53, v189, v218
	v_sub_f32_e32 v54, v190, v218
	v_sub_f32_e32 v55, v191, v218
	s_waitcnt lgkmcnt(3)
	ds_read_b128 v[156:159], v144 offset:6144
	ds_read_b128 v[148:151], v144 offset:6656
	v_mfma_f32_32x32x16_f16 v[0:15], v[136:139], v[184:187], v[0:15]
	v_exp_f32_e32 v68, v68
	v_exp_f32_e32 v69, v69
	v_exp_f32_e32 v70, v70
	v_exp_f32_e32 v71, v71
	v_sub_f32_e32 v56, v56, v218
	v_sub_f32_e32 v57, v57, v218
	v_sub_f32_e32 v58, v58, v218
	v_sub_f32_e32 v59, v59, v218
	v_sub_f32_e32 v60, v60, v218
	v_sub_f32_e32 v61, v61, v218
	v_sub_f32_e32 v62, v62, v218
	v_sub_f32_e32 v63, v63, v218
	s_nop 0
	v_mfma_f32_32x32x16_f16 v[16:31], v[132:135], v[32:35], v[16:31]
	v_exp_f32_e32 v72, v72
	v_exp_f32_e32 v73, v73
	v_exp_f32_e32 v74, v74
	v_exp_f32_e32 v75, v75
	v_sub_f32_e32 v32, v36, v218
	v_sub_f32_e32 v33, v37, v218
	v_sub_f32_e32 v34, v38, v218
	v_sub_f32_e32 v35, v39, v218
	v_sub_f32_e32 v36, v198, v218
	v_sub_f32_e32 v37, v199, v218
	v_sub_f32_e32 v38, v200, v218
	v_sub_f32_e32 v39, v201, v218
	s_waitcnt lgkmcnt(4)
	v_mfma_f32_32x32x16_f16 v[0:15], v[132:135], v[180:183], v[0:15]
	v_exp_f32_e32 v76, v76
	v_exp_f32_e32 v77, v77
	v_exp_f32_e32 v78, v78
	v_exp_f32_e32 v79, v79
	v_sub_f32_e32 v40, v40, v218
	v_sub_f32_e32 v41, v41, v218
	v_sub_f32_e32 v42, v42, v218
	v_sub_f32_e32 v43, v43, v218
	v_sub_f32_e32 v44, v44, v218
	v_sub_f32_e32 v45, v45, v218
	v_sub_f32_e32 v46, v46, v218
	v_sub_f32_e32 v47, v47, v218
	s_nop 0
	s_waitcnt vmcnt(2) lgkmcnt(0)
	s_barrier
	s_andn2_b64 vcc, exec, s[40:41]
	s_cbranch_vccnz .LBB0_635
	s_waitcnt lgkmcnt(0)
	ds_read_b128 v[180:183], v227 offset:49248
	ds_read_b128 v[184:187], v227 offset:49216
	ds_read_b128 v[188:191], v227 offset:49184
	ds_read_b128 v[198:201], v227 offset:49152
	s_waitcnt lgkmcnt(3)
	v_pk_mul_f32 v[30:31], v[30:31], v[182:183]
	s_waitcnt lgkmcnt(2)
	v_pk_mul_f32 v[26:27], v[26:27], v[186:187]
	s_waitcnt lgkmcnt(1)
	v_pk_mul_f32 v[22:23], v[22:23], v[190:191]
	s_waitcnt lgkmcnt(0)
	v_pk_mul_f32 v[18:19], v[18:19], v[200:201]
	v_pk_mul_f32 v[28:29], v[28:29], v[180:181]
	v_pk_mul_f32 v[24:25], v[24:25], v[184:185]
	v_pk_mul_f32 v[20:21], v[20:21], v[188:189]
	v_pk_mul_f32 v[16:17], v[16:17], v[198:199]
	v_pk_mul_f32 v[14:15], v[14:15], v[182:183]
	v_pk_mul_f32 v[10:11], v[10:11], v[186:187]
	v_pk_mul_f32 v[6:7], v[6:7], v[190:191]
	v_pk_mul_f32 v[2:3], v[2:3], v[200:201]
	v_pk_mul_f32 v[12:13], v[12:13], v[180:181]
	v_pk_mul_f32 v[8:9], v[8:9], v[184:185]
	v_pk_mul_f32 v[4:5], v[4:5], v[188:189]
	v_pk_mul_f32 v[0:1], v[0:1], v[198:199]

; #define WAIT_BAR(N) asm volatile("s_waitcnt vmcnt(" #N ") lgkmcnt(0)\n\ts_barrier" ::: "memory")
; #define RESC() do { if (resc) { asm volatile("s_waitcnt lgkmcnt(0)" ::: "memory"); \
;       _Pragma("unroll") for (int d_ = 0; d_ < 2; ++d_) _Pragma("unroll") for (int r = 0; r < 16; ++r) o[d_][r] *= wsf[crow(r, hi)]; } } while (0)
; #define ROT() do { sl_prev = sl_cur; sl_cur = sl_next; sl_next = (sl_next == (NSLOT - 1) * SLOTB) ? 0 : sl_next + SLOTB; } while (0)
; #define ENDW(tt) do { if ((tt) + 3 < NT) { WAIT_BAR(2); } else if ((tt) + 2 < NT) { WAIT_BAR(1); } else { WAIT_BAR(0); } } while (0)
; template <bool MOBA, int THRL> ...
;     ...
;     int t = 1;
;     ...
;     for (; t + 5 < NT; t += 2) {
;         STEP(pB0, pB1, pA0, pA1, t, true, true, true);       WAIT_BAR(2); RESC(); ROT();
;         STEP(pA0, pA1, pB0, pB1, t + 1, true, true, true);   WAIT_BAR(2); RESC(); ROT();
;     }
;     for (; t + 1 < NT; t += 2) {
;         STEP(pB0, pB1, pA0, pA1, t, (t + 3 < NT), (t + 1 < NT), (t + 1 < NT));       ENDW(t);     RESC(); ROT();
;         STEP(pA0, pA1, pB0, pB1, t + 1, (t + 4 < NT), (t + 2 < NT), (t + 2 < NT));   ENDW(t + 1); RESC(); ROT();
.LBB0_651:
	s_waitcnt lgkmcnt(14)
	v_mfma_f32_32x32x16_f16 v[16:31], v[144:147], v[192:195], v[16:31]
	v_exp_f32_e32 v48, v48
	v_exp_f32_e32 v49, v49
	v_exp_f32_e32 v50, v50
	v_exp_f32_e32 v51, v51
	v_lshl_add_u32 v76, s45, 8, v232
	ds_read_b128 v[148:151], v76
	ds_read_b128 v[68:71], v76 offset:128
	s_waitcnt lgkmcnt(14)
	v_mfma_f32_32x32x16_f16 v[0:15], v[144:147], v[176:179], v[0:15]
	v_exp_f32_e32 v52, v52
	v_exp_f32_e32 v53, v53
	v_exp_f32_e32 v54, v54
	v_exp_f32_e32 v55, v55
	ds_read_b128 v[156:159], v76 offset:32
	ds_read_b128 v[192:195], v76 offset:160
	v_add_u32_e32 v144, s18, v230
	ds_read_b128 v[176:179], v144
	ds_read_b128 v[172:175], v144 offset:512
	s_waitcnt lgkmcnt(14)
	v_mfma_f32_32x32x16_f16 v[16:31], v[140:143], v[188:191], v[16:31]
	v_exp_f32_e32 v56, v56
	v_exp_f32_e32 v57, v57
	v_exp_f32_e32 v58, v58
	v_exp_f32_e32 v59, v59
	ds_read_b128 v[88:91], v76 offset:64
	ds_read_b128 v[72:75], v76 offset:192
	ds_read_b128 v[168:171], v144 offset:2048
	ds_read_b128 v[164:167], v144 offset:2560
	v_mfma_f32_32x32x16_f16 v[0:15], v[140:143], v[84:87], v[0:15]
	v_exp_f32_e32 v60, v60
	v_exp_f32_e32 v61, v61
	v_exp_f32_e32 v62, v62
	v_exp_f32_e32 v63, v63
	ds_read_b128 v[92:95], v76 offset:96
	ds_read_b128 v[76:79], v76 offset:224
	ds_read_b128 v[160:163], v144 offset:4096
	ds_read_b128 v[152:155], v144 offset:4608
	s_waitcnt lgkmcnt(14)
	v_mfma_f32_32x32x16_f16 v[16:31], v[136:139], v[80:83], v[16:31]
	v_exp_f32_e32 v32, v32
	v_exp_f32_e32 v33, v33
	v_exp_f32_e32 v34, v34
	v_exp_f32_e32 v35, v35
	s_waitcnt lgkmcnt(13)
	v_sub_f32_e32 v80, v148, v218
	v_sub_f32_e32 v81, v149, v218
	v_sub_f32_e32 v82, v150, v218
	v_sub_f32_e32 v83, v151, v218
	s_waitcnt lgkmcnt(11)
	v_sub_f32_e32 v84, v156, v218
	v_sub_f32_e32 v85, v157, v218
	v_sub_f32_e32 v86, v158, v218
	v_sub_f32_e32 v87, v159, v218
	s_waitcnt lgkmcnt(3)
	ds_read_b128 v[156:159], v144 offset:6144
	ds_read_b128 v[148:151], v144 offset:6656
	v_mfma_f32_32x32x16_f16 v[0:15], v[136:139], v[184:187], v[0:15]
	v_exp_f32_e32 v36, v36
	v_exp_f32_e32 v37, v37
	v_exp_f32_e32 v38, v38
	v_exp_f32_e32 v39, v39
	v_sub_f32_e32 v88, v88, v218
	v_sub_f32_e32 v89, v89, v218
	v_sub_f32_e32 v90, v90, v218
	v_sub_f32_e32 v91, v91, v218
	v_sub_f32_e32 v92, v92, v218
	v_sub_f32_e32 v93, v93, v218
	v_sub_f32_e32 v94, v94, v218
	v_sub_f32_e32 v95, v95, v218
	s_nop 0
	v_mfma_f32_32x32x16_f16 v[16:31], v[132:135], v[64:67], v[16:31]
	v_exp_f32_e32 v40, v40
	v_exp_f32_e32 v41, v41
	v_exp_f32_e32 v42, v42
	v_exp_f32_e32 v43, v43
	v_sub_f32_e32 v64, v68, v218
	v_sub_f32_e32 v65, v69, v218
	v_sub_f32_e32 v66, v70, v218
	v_sub_f32_e32 v67, v71, v218
	v_sub_f32_e32 v68, v192, v218
	v_sub_f32_e32 v69, v193, v218
	v_sub_f32_e32 v70, v194, v218
	v_sub_f32_e32 v71, v195, v218
	s_waitcnt lgkmcnt(4)
	v_mfma_f32_32x32x16_f16 v[0:15], v[132:135], v[180:183], v[0:15]
	v_exp_f32_e32 v44, v44
	v_exp_f32_e32 v45, v45
	v_exp_f32_e32 v46, v46
	v_exp_f32_e32 v47, v47
	v_sub_f32_e32 v72, v72, v218
	v_sub_f32_e32 v73, v73, v218
	v_sub_f32_e32 v74, v74, v218
	v_sub_f32_e32 v75, v75, v218
	v_sub_f32_e32 v76, v76, v218
	v_sub_f32_e32 v77, v77, v218
	v_sub_f32_e32 v78, v78, v218
	v_sub_f32_e32 v79, v79, v218
	s_nop 0
	s_mov_b64 s[68:69], -1
	s_and_b64 vcc, exec, s[50:51]
	s_cbranch_vccnz .LBB0_692
	s_andn2_b64 vcc, exec, s[68:69]
	s_cbranch_vccz .LBB0_697
